# T3 (norm2 + router): packed f32 VALU ops split into single-lane ops (613 sites)
# speedup vs baseline: 1.0037x; 1.0037x over previous
.LBB0_1068:
	s_mul_hi_i32 s2, s10, 0x38e38e39
	s_lshr_b32 s3, s2, 31
	s_ashr_i32 s2, s2, 9
	s_add_i32 s2, s2, s3
	s_mul_i32 s3, s2, 0xfffff700
	s_add_i32 s3, s10, s3
	s_cmpk_lt_i32 s3, 0x100
	s_cselect_b64 s[14:15], -1, 0
	s_and_b64 s[16:17], s[0:1], s[14:15]
	s_and_b64 vcc, exec, s[16:17]
	s_cbranch_vccnz .LBB0_1067
	s_and_b64 s[14:15], s[14:15], exec
	s_cselect_b32 s2, 8, s2
	s_cmp_eq_u32 s2, s23
	s_cbranch_scc1 .LBB0_1071
	s_load_dwordx2 s[14:15], s[8:9], 0x38
	s_mul_i32 s11, s2, 0xc000
	s_mul_hi_i32 s3, s2, 0xc000
	s_add_u32 s11, s21, s11
	s_addc_u32 s3, s22, s3
	s_waitcnt lgkmcnt(0)
	s_add_u32 s14, s14, s12
	s_addc_u32 s15, s15, s13
	s_add_u32 s16, s11, 0x8000
	s_addc_u32 s17, s3, 0
	global_load_dwordx4 v[32:35], v205, s[16:17]
	global_load_dwordx4 v[36:39], v206, s[16:17]
	global_load_dwordx4 v[40:43], v207, s[16:17]
	global_load_dwordx4 v[44:47], v208, s[16:17]
	global_load_dwordx4 v[48:51], v209, s[16:17]
	global_load_dwordx4 v[52:55], v210, s[16:17]
	global_load_dwordx4 v[56:59], v211, s[16:17]
	global_load_dwordx4 v[60:63], v212, s[16:17]
	global_load_dwordx4 v[70:73], v205, s[14:15]
	global_load_dwordx4 v[74:77], v205, s[14:15] offset:1024
	global_load_dwordx4 v[78:81], v205, s[14:15] offset:2048
	global_load_dwordx4 v[82:85], v205, s[14:15] offset:3072
	global_load_dwordx4 v[86:89], v209, s[14:15]
	global_load_dwordx4 v[90:93], v210, s[14:15]
	global_load_dwordx4 v[94:97], v211, s[14:15]
	global_load_dwordx4 v[98:101], v212, s[14:15]
	s_add_u32 s14, s11, 0x6000
	s_addc_u32 s15, s3, 0
	global_load_dwordx4 v[0:3], v205, s[14:15]
	global_load_dwordx4 v[4:7], v206, s[14:15]
	global_load_dwordx4 v[8:11], v207, s[14:15]
	global_load_dwordx4 v[12:15], v208, s[14:15]
	global_load_dwordx4 v[16:19], v209, s[14:15]
	global_load_dwordx4 v[20:23], v210, s[14:15]
	global_load_dwordx4 v[24:27], v211, s[14:15]
	global_load_dwordx4 v[28:31], v212, s[14:15]
	s_mov_b32 s23, s2
	s_waitcnt vmcnt(23)
	v_add_f32_e32 v34, 1.0, v34
	v_add_f32_e32 v35, 1.0, v35
	v_add_f32_e32 v32, 1.0, v32
	v_add_f32_e32 v33, 1.0, v33
	s_waitcnt vmcnt(22)
	v_add_f32_e32 v38, 1.0, v38
	v_add_f32_e32 v39, 1.0, v39
	v_add_f32_e32 v36, 1.0, v36
	v_add_f32_e32 v37, 1.0, v37
	s_waitcnt vmcnt(21)
	v_add_f32_e32 v42, 1.0, v42
	v_add_f32_e32 v43, 1.0, v43
	v_add_f32_e32 v40, 1.0, v40
	v_add_f32_e32 v41, 1.0, v41
	s_waitcnt vmcnt(20)
	v_add_f32_e32 v46, 1.0, v46
	v_add_f32_e32 v47, 1.0, v47
	v_add_f32_e32 v44, 1.0, v44
	v_add_f32_e32 v45, 1.0, v45
	s_waitcnt vmcnt(19)
	v_add_f32_e32 v50, 1.0, v50
	v_add_f32_e32 v51, 1.0, v51
	v_add_f32_e32 v48, 1.0, v48
	v_add_f32_e32 v49, 1.0, v49
	s_waitcnt vmcnt(18)
	v_add_f32_e32 v54, 1.0, v54
	v_add_f32_e32 v55, 1.0, v55
	v_add_f32_e32 v52, 1.0, v52
	v_add_f32_e32 v53, 1.0, v53
	s_waitcnt vmcnt(17)
	v_add_f32_e32 v58, 1.0, v58
	v_add_f32_e32 v59, 1.0, v59
	v_add_f32_e32 v56, 1.0, v56
	v_add_f32_e32 v57, 1.0, v57
	s_waitcnt vmcnt(16)
	v_add_f32_e32 v62, 1.0, v62
	v_add_f32_e32 v63, 1.0, v63
	v_add_f32_e32 v60, 1.0, v60
	v_add_f32_e32 v61, 1.0, v61
	s_waitcnt vmcnt(15)
	v_mul_f32_e32 v34, v72, v34
	v_mul_f32_e32 v35, v73, v35
	v_mul_f32_e32 v32, v70, v32
	v_mul_f32_e32 v33, v71, v33
	s_waitcnt vmcnt(14)
	v_mul_f32_e32 v38, v76, v38
	v_mul_f32_e32 v39, v77, v39
	v_mul_f32_e32 v36, v74, v36
	v_mul_f32_e32 v37, v75, v37
	s_waitcnt vmcnt(13)
	v_mul_f32_e32 v42, v80, v42
	v_mul_f32_e32 v43, v81, v43
	v_mul_f32_e32 v40, v78, v40
	v_mul_f32_e32 v41, v79, v41
	s_waitcnt vmcnt(12)
	v_mul_f32_e32 v46, v84, v46
	v_mul_f32_e32 v47, v85, v47
	v_mul_f32_e32 v44, v82, v44
	v_mul_f32_e32 v45, v83, v45
	s_waitcnt vmcnt(11)
	v_mul_f32_e32 v50, v88, v50
	v_mul_f32_e32 v51, v89, v51
	v_mul_f32_e32 v48, v86, v48
	v_mul_f32_e32 v49, v87, v49
	s_waitcnt vmcnt(10)
	v_mul_f32_e32 v54, v92, v54
	v_mul_f32_e32 v55, v93, v55
	v_mul_f32_e32 v52, v90, v52
	v_mul_f32_e32 v53, v91, v53
	s_waitcnt vmcnt(9)
	v_mul_f32_e32 v58, v96, v58
	v_mul_f32_e32 v59, v97, v59
	v_mul_f32_e32 v56, v94, v56
	v_mul_f32_e32 v57, v95, v57
	s_waitcnt vmcnt(8)
	v_mul_f32_e32 v62, v100, v62
	v_mul_f32_e32 v63, v101, v63
	v_mul_f32_e32 v60, v98, v60
	v_mul_f32_e32 v61, v99, v61
.LBB0_1071:
	s_ashr_i32 s11, s10, 31
	s_lshl_b64 s[2:3], s[10:11], 12
	v_lshl_add_u64 v[70:71], v[66:67], 0, s[2:3]
	global_load_dwordx2 v[72:73], v[70:71], off
	global_load_dwordx2 v[74:75], v[70:71], off offset:512
	global_load_dwordx2 v[78:79], v[70:71], off offset:1024
	global_load_dwordx2 v[82:83], v[70:71], off offset:1536
	global_load_dwordx2 v[84:85], v[70:71], off offset:2048
	global_load_dwordx2 v[88:89], v[70:71], off offset:2560
	global_load_dwordx2 v[94:95], v[70:71], off offset:3072
	s_add_i32 s14, s10, 1
	global_load_dwordx2 v[70:71], v[70:71], off offset:3584
	s_ashr_i32 s15, s14, 31
	s_lshl_b64 s[2:3], s[14:15], 12
	v_lshl_add_u64 v[76:77], v[66:67], 0, s[2:3]
	global_load_dwordx2 v[96:97], v[76:77], off
	global_load_dwordx2 v[104:105], v[76:77], off offset:512
	global_load_dwordx2 v[106:107], v[76:77], off offset:1024
	global_load_dwordx2 v[118:119], v[76:77], off offset:1536
	global_load_dwordx2 v[122:123], v[76:77], off offset:2048
	global_load_dwordx2 v[126:127], v[76:77], off offset:2560
	global_load_dwordx2 v[132:133], v[76:77], off offset:3072
	global_load_dwordx2 v[136:137], v[76:77], off offset:3584
	s_mov_b32 s2, 0x3a000000
	s_waitcnt vmcnt(15)
	v_lshlrev_b32_e32 v214, 16, v72
	v_and_b32_e32 v215, 0xffff0000, v72
	v_lshlrev_b32_e32 v72, 16, v73
	v_and_b32_e32 v73, 0xffff0000, v73
	s_waitcnt vmcnt(11)
	v_lshlrev_b32_e32 v92, 16, v84
	v_and_b32_e32 v93, 0xffff0000, v84
	v_lshlrev_b32_e32 v90, 16, v85
	v_and_b32_e32 v91, 0xffff0000, v85
	v_mul_f32_e32 v84, v215, v215
	v_mul_f32_e32 v85, v73, v73
	v_lshlrev_b32_e32 v76, 16, v74
	v_and_b32_e32 v77, 0xffff0000, v74
	v_lshlrev_b32_e32 v74, 16, v75
	v_and_b32_e32 v75, 0xffff0000, v75
	v_fmac_f32_e32 v84, v214, v214
	v_fmac_f32_e32 v85, v72, v72
	s_waitcnt vmcnt(10)
	v_lshlrev_b32_e32 v100, 16, v88
	v_and_b32_e32 v101, 0xffff0000, v88
	v_add_f32_e32 v84, v84, v85
	v_mul_f32_e32 v85, v77, v77
	v_mul_f32_e32 v88, v75, v75
	v_fmac_f32_e32 v85, v76, v76
	v_fmac_f32_e32 v88, v74, v74
	v_lshlrev_b32_e32 v80, 16, v78
	v_and_b32_e32 v81, 0xffff0000, v78
	v_lshlrev_b32_e32 v78, 16, v79
	v_and_b32_e32 v79, 0xffff0000, v79
	v_add_f32_e32 v85, v85, v88
	v_add_f32_e32 v84, v84, v85
	v_mul_f32_e32 v85, v81, v81
	v_mul_f32_e32 v88, v79, v79
	v_fmac_f32_e32 v85, v80, v80
	v_fmac_f32_e32 v88, v78, v78
	v_lshlrev_b32_e32 v86, 16, v82
	v_and_b32_e32 v87, 0xffff0000, v82
	v_lshlrev_b32_e32 v82, 16, v83
	v_and_b32_e32 v83, 0xffff0000, v83
	v_add_f32_e32 v85, v85, v88
	v_add_f32_e32 v84, v84, v85
	v_mul_f32_e32 v85, v87, v87
	v_mul_f32_e32 v88, v83, v83
	v_fmac_f32_e32 v85, v86, v86
	v_fmac_f32_e32 v88, v82, v82
	v_add_f32_e32 v85, v85, v88
	v_add_f32_e32 v84, v84, v85
	v_mul_f32_e32 v85, v93, v93
	v_mul_f32_e32 v88, v91, v91
	v_fmac_f32_e32 v85, v92, v92
	v_fmac_f32_e32 v88, v90, v90
	v_and_b32_e32 v99, 0xffff0000, v89
	v_add_f32_e32 v85, v85, v88
	v_lshlrev_b32_e32 v98, 16, v89
	v_add_f32_e32 v84, v84, v85
	v_mul_f32_e32 v85, v101, v101
	v_mul_f32_e32 v88, v99, v99
	v_fmac_f32_e32 v85, v100, v100
	v_fmac_f32_e32 v88, v98, v98
	s_waitcnt vmcnt(9)
	v_and_b32_e32 v109, 0xffff0000, v94
	v_and_b32_e32 v103, 0xffff0000, v95
	v_add_f32_e32 v85, v85, v88
	v_lshlrev_b32_e32 v108, 16, v94
	v_lshlrev_b32_e32 v102, 16, v95
	v_add_f32_e32 v84, v84, v85
	v_mul_f32_e32 v85, v109, v109
	v_mul_f32_e32 v88, v103, v103
	v_fmac_f32_e32 v85, v108, v108
	v_fmac_f32_e32 v88, v102, v102
	s_waitcnt vmcnt(8)
	v_and_b32_e32 v117, 0xffff0000, v70
	v_and_b32_e32 v113, 0xffff0000, v71
	v_add_f32_e32 v85, v85, v88
	v_lshlrev_b32_e32 v116, 16, v70
	v_lshlrev_b32_e32 v112, 16, v71
	v_add_f32_e32 v84, v84, v85
	v_mul_f32_e32 v85, v117, v117
	v_mul_f32_e32 v88, v113, v113
	v_fmac_f32_e32 v85, v116, v116
	v_fmac_f32_e32 v88, v112, v112
	v_add_f32_e32 v85, v85, v88
	v_add_f32_e32 v84, v84, v85
	s_waitcnt vmcnt(7)
	v_and_b32_e32 v71, 0xffff0000, v96
	v_and_b32_e32 v95, 0xffff0000, v97
	v_add_f32_dpp v84, v84, v84 quad_perm:[1,0,3,2] row_mask:0xf bank_mask:0xf bound_ctrl:1
	v_lshlrev_b32_e32 v70, 16, v96
	v_lshlrev_b32_e32 v94, 16, v97
	v_add_f32_dpp v84, v84, v84 quad_perm:[2,3,0,1] row_mask:0xf bank_mask:0xf bound_ctrl:1
	v_mul_f32_e32 v88, v95, v95
	s_waitcnt vmcnt(6)
	v_lshlrev_b32_e32 v216, 16, v104
	v_add_f32_dpp v84, v84, v84 row_half_mirror row_mask:0xf bank_mask:0xf bound_ctrl:1
	v_and_b32_e32 v217, 0xffff0000, v104
	v_lshlrev_b32_e32 v104, 16, v105
	v_add_f32_dpp v84, v84, v84 row_mirror row_mask:0xf bank_mask:0xf bound_ctrl:1
	v_mov_b32_e32 v85, v84
	s_nop 1
	v_permlane16_swap_b32_e32 v84, v85
	v_add_f32_e32 v85, v84, v85
	v_mul_f32_e32 v84, v71, v71
	v_and_b32_e32 v105, 0xffff0000, v105
	v_fmac_f32_e32 v84, v70, v70
	v_fmac_f32_e32 v88, v94, v94
	v_add_f32_e32 v84, v84, v88
	v_mul_f32_e32 v88, v217, v217
	v_mul_f32_e32 v96, v105, v105
	v_fmac_f32_e32 v88, v216, v216
	v_fmac_f32_e32 v96, v104, v104
	s_waitcnt vmcnt(5)
	v_and_b32_e32 v115, 0xffff0000, v106
	v_and_b32_e32 v111, 0xffff0000, v107
	v_add_f32_e32 v88, v88, v96
	v_lshlrev_b32_e32 v114, 16, v106
	v_lshlrev_b32_e32 v110, 16, v107
	v_add_f32_e32 v84, v84, v88
	v_mul_f32_e32 v88, v115, v115
	v_mul_f32_e32 v96, v111, v111
	v_fmac_f32_e32 v88, v114, v114
	v_fmac_f32_e32 v96, v110, v110
	s_waitcnt vmcnt(4)
	v_lshlrev_b32_e32 v120, 16, v118
	v_and_b32_e32 v121, 0xffff0000, v118
	v_lshlrev_b32_e32 v118, 16, v119
	v_and_b32_e32 v119, 0xffff0000, v119
	v_add_f32_e32 v88, v88, v96
	v_add_f32_e32 v84, v84, v88
	v_mul_f32_e32 v88, v121, v121
	v_mul_f32_e32 v96, v119, v119
	v_fmac_f32_e32 v88, v120, v120
	v_fmac_f32_e32 v96, v118, v118
	s_waitcnt vmcnt(3)
	v_lshlrev_b32_e32 v124, 16, v122
	v_and_b32_e32 v125, 0xffff0000, v122
	v_lshlrev_b32_e32 v122, 16, v123
	v_and_b32_e32 v123, 0xffff0000, v123
	v_add_f32_e32 v88, v88, v96
	v_add_f32_e32 v84, v84, v88
	v_mul_f32_e32 v88, v125, v125
	v_mul_f32_e32 v96, v123, v123
	v_fmac_f32_e32 v88, v124, v124
	v_fmac_f32_e32 v96, v122, v122
	s_waitcnt vmcnt(2)
	v_lshlrev_b32_e32 v130, 16, v126
	v_and_b32_e32 v131, 0xffff0000, v126
	v_lshlrev_b32_e32 v126, 16, v127
	v_and_b32_e32 v127, 0xffff0000, v127
	v_add_f32_e32 v88, v88, v96
	v_add_f32_e32 v84, v84, v88
	v_mul_f32_e32 v88, v131, v131
	v_mul_f32_e32 v96, v127, v127
	v_fmac_f32_e32 v88, v130, v130
	v_fmac_f32_e32 v96, v126, v126
	s_waitcnt vmcnt(1)
	v_lshlrev_b32_e32 v134, 16, v132
	v_and_b32_e32 v135, 0xffff0000, v132
	v_lshlrev_b32_e32 v132, 16, v133
	v_and_b32_e32 v133, 0xffff0000, v133
	v_add_f32_e32 v88, v88, v96
	v_add_f32_e32 v84, v84, v88
	v_mul_f32_e32 v88, v135, v135
	v_mul_f32_e32 v96, v133, v133
	v_fmac_f32_e32 v88, v134, v134
	v_fmac_f32_e32 v96, v132, v132
	s_waitcnt vmcnt(0)
	v_lshlrev_b32_e32 v138, 16, v136
	v_and_b32_e32 v139, 0xffff0000, v136
	v_lshlrev_b32_e32 v136, 16, v137
	v_and_b32_e32 v137, 0xffff0000, v137
	v_add_f32_e32 v88, v88, v96
	v_add_f32_e32 v84, v84, v88
	v_mul_f32_e32 v88, v139, v139
	v_mul_f32_e32 v96, v137, v137
	v_fmac_f32_e32 v88, v138, v138
	v_fmac_f32_e32 v96, v136, v136
	v_add_f32_e32 v88, v88, v96
	v_add_f32_e32 v84, v84, v88
	v_mov_b32_e32 v89, v85
	s_nop 1
	v_permlane32_swap_b32_e32 v85, v89
	v_add_f32_dpp v84, v84, v84 quad_perm:[1,0,3,2] row_mask:0xf bank_mask:0xf bound_ctrl:1
	s_nop 1
	v_add_f32_dpp v84, v84, v84 quad_perm:[2,3,0,1] row_mask:0xf bank_mask:0xf bound_ctrl:1
	s_nop 1
	v_add_f32_dpp v84, v84, v84 row_half_mirror row_mask:0xf bank_mask:0xf bound_ctrl:1
	s_nop 1
	v_add_f32_dpp v84, v84, v84 row_mirror row_mask:0xf bank_mask:0xf bound_ctrl:1
	v_mov_b32_e32 v88, v84
	s_nop 1
	v_permlane16_swap_b32_e32 v84, v88
	v_add_f32_e32 v84, v84, v88
	v_mov_b32_e32 v88, v84
	s_nop 1
	v_permlane32_swap_b32_e32 v84, v88
	v_add_f32_e32 v84, v84, v88
	v_add_f32_e32 v85, v85, v89
	s_nop 0
	v_pk_fma_f32 v[84:85], v[84:85], s[2:3], v[248:249] op_sel_hi:[1,0,0]
	s_mov_b32 s2, 0x800000
	v_mul_f32_e32 v88, 0x4b800000, v85
	v_cmp_gt_f32_e32 vcc, s2, v85
	v_cmp_gt_f32_e64 s[70:71], s2, v84
	s_nop 0
	v_cndmask_b32_e32 v85, v85, v88, vcc
	v_mul_f32_e32 v88, 0x4b800000, v84
	v_rsq_f32_e32 v85, v85
	v_cndmask_b32_e64 v84, v84, v88, s[70:71]
	v_rsq_f32_e32 v84, v84
	v_mul_f32_e32 v88, 0x45800000, v85
	v_cndmask_b32_e32 v128, v85, v88, vcc
	v_mul_f32_e32 v85, 0x45800000, v84
	v_cndmask_b32_e64 v218, v84, v85, s[70:71]
	v_mul_f32_e32 v76, v128, v76
	v_mul_f32_e32 v77, v128, v77
	v_mul_f32_e32 v88, v128, v214
	v_mul_f32_e32 v89, v128, v215
	v_fma_f32 v96, v76, v36, v4
	v_fma_f32 v97, v77, v37, v5
	v_mul_f32_e32 v76, v218, v216
	v_mul_f32_e32 v77, v218, v217
	ds_read_b128 v[214:217], v65
	v_mul_f32_e32 v72, v128, v72
	v_mul_f32_e32 v73, v128, v73
	v_mul_f32_e32 v74, v128, v74
	v_mul_f32_e32 v75, v128, v75
	v_mul_f32_e32 v80, v128, v80
	v_mul_f32_e32 v81, v128, v81
	v_mul_f32_e32 v78, v128, v78
	v_mul_f32_e32 v79, v128, v79
	v_mul_f32_e32 v86, v128, v86
	v_mul_f32_e32 v87, v128, v87
	v_mul_f32_e32 v82, v128, v82
	v_mul_f32_e32 v83, v128, v83
	v_mul_f32_e32 v92, v128, v92
	v_mul_f32_e32 v93, v128, v93
	v_mul_f32_e32 v90, v128, v90
	v_mul_f32_e32 v91, v128, v91
	v_mul_f32_e32 v100, v128, v100
	v_mul_f32_e32 v101, v128, v101
	v_mul_f32_e32 v98, v128, v98
	v_mul_f32_e32 v99, v128, v99
	v_mul_f32_e32 v108, v128, v108
	v_mul_f32_e32 v109, v128, v109
	v_mul_f32_e32 v102, v128, v102
	v_mul_f32_e32 v103, v128, v103
	v_mul_f32_e32 v116, v128, v116
	v_mul_f32_e32 v117, v128, v117
	v_mul_f32_e32 v112, v128, v112
	v_mul_f32_e32 v113, v128, v113
	v_fma_f32 v84, v72, v34, v2
	v_fma_f32 v85, v73, v35, v3
	v_mul_f32_e32 v72, v218, v70
	v_mul_f32_e32 v73, v218, v71
	v_mul_f32_e32 v70, v218, v94
	v_mul_f32_e32 v71, v218, v95
	v_fma_f32 v94, v74, v38, v6
	v_fma_f32 v95, v75, v39, v7
	v_mul_f32_e32 v74, v218, v104
	v_mul_f32_e32 v75, v218, v105
	v_fma_f32 v104, v78, v42, v10
	v_fma_f32 v105, v79, v43, v11
	v_fma_f32 v106, v80, v40, v8
	v_fma_f32 v107, v81, v41, v9
	v_mul_f32_e32 v80, v218, v114
	v_mul_f32_e32 v81, v218, v115
	v_mul_f32_e32 v78, v218, v110
	v_mul_f32_e32 v79, v218, v111
	v_fma_f32 v110, v82, v46, v14
	v_fma_f32 v111, v83, v47, v15
	v_fma_f32 v114, v86, v44, v12
	v_fma_f32 v115, v87, v45, v13
	v_mul_f32_e32 v86, v218, v120
	v_mul_f32_e32 v87, v218, v121
	v_mul_f32_e32 v82, v218, v118
	v_mul_f32_e32 v83, v218, v119
	v_fma_f32 v118, v90, v50, v18
	v_fma_f32 v119, v91, v51, v19
	v_fma_f32 v120, v92, v48, v16
	v_fma_f32 v121, v93, v49, v17
	v_mul_f32_e32 v92, v218, v124
	v_mul_f32_e32 v93, v218, v125
	v_mul_f32_e32 v90, v218, v122
	v_mul_f32_e32 v91, v218, v123
	v_fma_f32 v122, v98, v54, v22
	v_fma_f32 v123, v99, v55, v23
	v_fma_f32 v124, v100, v52, v20
	v_fma_f32 v125, v101, v53, v21
	v_mul_f32_e32 v100, v218, v130
	v_mul_f32_e32 v101, v218, v131
	v_mul_f32_e32 v98, v218, v126
	v_mul_f32_e32 v99, v218, v127
	v_fma_f32 v126, v102, v58, v26
	v_fma_f32 v127, v103, v59, v27
	v_fma_f32 v130, v108, v56, v24
	v_fma_f32 v131, v109, v57, v25
	v_mul_f32_e32 v108, v218, v134
	v_mul_f32_e32 v109, v218, v135
	v_mul_f32_e32 v102, v218, v132
	v_mul_f32_e32 v103, v218, v133
	v_fma_f32 v132, v112, v62, v30
	v_fma_f32 v133, v113, v63, v31
	v_fma_f32 v134, v116, v60, v28
	v_fma_f32 v135, v117, v61, v29
	v_mul_f32_e32 v116, v218, v138
	v_mul_f32_e32 v117, v218, v139
	v_mul_f32_e32 v112, v218, v136
	v_mul_f32_e32 v113, v218, v137
	ds_read_b128 v[136:139], v65 offset:1024
	v_fma_f32 v88, v88, v32, v0
	v_fma_f32 v89, v89, v33, v1
	v_fma_f32 v72, v32, v72, v0
	v_fma_f32 v73, v33, v73, v1
	v_fma_f32 v70, v34, v70, v2
	v_fma_f32 v71, v35, v71, v3
	s_waitcnt lgkmcnt(1)
	v_fma_f32 v218, v88, v214, 0
	v_fma_f32 v219, v89, v215, 0
	v_fma_f32 v214, v214, v72, 0
	v_fma_f32 v215, v215, v73, 0
	v_fma_f32 v76, v36, v76, v4
	v_fma_f32 v77, v37, v77, v5
	v_fmac_f32_e32 v218, v84, v216
	v_fmac_f32_e32 v219, v85, v217
	v_fma_f32 v220, v216, v70, v214
	v_fma_f32 v221, v217, v71, v215
	ds_read_b128 v[214:217], v65 offset:2048
	v_fma_f32 v74, v38, v74, v6
	v_fma_f32 v75, v39, v75, v7
	s_waitcnt lgkmcnt(1)
	v_fmac_f32_e32 v218, v96, v136
	v_fmac_f32_e32 v219, v97, v137
	v_fma_f32 v136, v136, v76, v220
	v_fma_f32 v137, v137, v77, v221
	v_fmac_f32_e32 v218, v94, v138
	v_fmac_f32_e32 v219, v95, v139
	v_fma_f32 v220, v138, v74, v136
	v_fma_f32 v221, v139, v75, v137
	ds_read_b128 v[136:139], v65 offset:3072
	v_fma_f32 v80, v40, v80, v8
	v_fma_f32 v81, v41, v81, v9
	v_fma_f32 v78, v42, v78, v10
	v_fma_f32 v79, v43, v79, v11
	s_waitcnt lgkmcnt(1)
	v_fmac_f32_e32 v218, v106, v214
	v_fmac_f32_e32 v219, v107, v215
	v_fma_f32 v214, v214, v80, v220
	v_fma_f32 v215, v215, v81, v221
	v_fma_f32 v86, v44, v86, v12
	v_fma_f32 v87, v45, v87, v13
	v_fmac_f32_e32 v218, v104, v216
	v_fmac_f32_e32 v219, v105, v217
	v_fma_f32 v220, v216, v78, v214
	v_fma_f32 v221, v217, v79, v215
	ds_read_b128 v[214:217], v65 offset:4096
	v_fma_f32 v82, v46, v82, v14
	v_fma_f32 v83, v47, v83, v15
	s_waitcnt lgkmcnt(1)
	v_fmac_f32_e32 v218, v114, v136
	v_fmac_f32_e32 v219, v115, v137
	v_fma_f32 v136, v136, v86, v220
	v_fma_f32 v137, v137, v87, v221
	v_fmac_f32_e32 v218, v110, v138
	v_fmac_f32_e32 v219, v111, v139
	v_fma_f32 v220, v138, v82, v136
	v_fma_f32 v221, v139, v83, v137
	ds_read_b128 v[136:139], v65 offset:5120
	v_fma_f32 v92, v48, v92, v16
	v_fma_f32 v93, v49, v93, v17
	v_fma_f32 v90, v50, v90, v18
	v_fma_f32 v91, v51, v91, v19
	s_waitcnt lgkmcnt(1)
	v_fmac_f32_e32 v218, v120, v214
	v_fmac_f32_e32 v219, v121, v215
	v_fma_f32 v214, v214, v92, v220
	v_fma_f32 v215, v215, v93, v221
	v_fma_f32 v100, v52, v100, v20
	v_fma_f32 v101, v53, v101, v21
	v_fmac_f32_e32 v218, v118, v216
	v_fmac_f32_e32 v219, v119, v217
	v_fma_f32 v220, v216, v90, v214
	v_fma_f32 v221, v217, v91, v215
	ds_read_b128 v[214:217], v65 offset:6144
	v_fma_f32 v98, v54, v98, v22
	v_fma_f32 v99, v55, v99, v23
	s_waitcnt lgkmcnt(1)
	v_fmac_f32_e32 v218, v124, v136
	v_fmac_f32_e32 v219, v125, v137
	v_fma_f32 v136, v136, v100, v220
	v_fma_f32 v137, v137, v101, v221
	v_fmac_f32_e32 v218, v122, v138
	v_fmac_f32_e32 v219, v123, v139
	v_fma_f32 v220, v138, v98, v136
	v_fma_f32 v221, v139, v99, v137
	ds_read_b128 v[136:139], v65 offset:7168
	v_fma_f32 v108, v56, v108, v24
	v_fma_f32 v109, v57, v109, v25
	s_waitcnt lgkmcnt(1)
	v_fmac_f32_e32 v218, v130, v214
	v_fmac_f32_e32 v219, v131, v215
	v_fma_f32 v102, v58, v102, v26
	v_fma_f32 v103, v59, v103, v27
	v_fmac_f32_e32 v218, v126, v216
	v_fmac_f32_e32 v219, v127, v217
	v_fma_f32 v214, v214, v108, v220
	v_fma_f32 v215, v215, v109, v221
	v_fma_f32 v116, v60, v116, v28
	v_fma_f32 v117, v61, v117, v29
	v_fmac_f32_e32 v214, v216, v102
	v_fmac_f32_e32 v215, v217, v103
	s_waitcnt lgkmcnt(0)
	v_fma_f32 v216, v134, v136, v218
	v_fma_f32 v217, v135, v137, v219
	v_fma_f32 v112, v62, v112, v30
	v_fma_f32 v113, v63, v113, v31
	v_fmac_f32_e32 v216, v132, v138
	v_fmac_f32_e32 v217, v133, v139
	v_fma_f32 v136, v136, v116, v214
	v_fma_f32 v137, v137, v117, v215
	v_add_f32_e32 v128, v216, v217
	ds_read_b128 v[214:217], v65 offset:15360
	ds_read_b128 v[218:221], v65 offset:14336
	ds_read_b128 v[222:225], v65 offset:9216
	ds_read_b128 v[226:229], v65 offset:8192
	ds_read_b128 v[234:237], v65 offset:13312
	ds_read_b128 v[238:241], v65 offset:12288
	ds_read_b128 v[242:245], v65 offset:11264
	ds_read_b128 v[246:249], v65 offset:10240
	v_fmac_f32_e32 v136, v138, v112
	v_fmac_f32_e32 v137, v139, v113
	s_waitcnt lgkmcnt(4)
	v_fma_f32 v138, v88, v226, 0
	v_fma_f32 v139, v89, v227, 0
	v_fma_f32 v226, v226, v72, 0
	v_fma_f32 v227, v227, v73, 0
	v_fmac_f32_e32 v138, v84, v228
	v_fmac_f32_e32 v139, v85, v229
	v_fmac_f32_e32 v226, v228, v70
	v_fmac_f32_e32 v227, v229, v71
	v_fmac_f32_e32 v138, v96, v222
	v_fmac_f32_e32 v139, v97, v223
	v_fma_f32 v222, v222, v76, v226
	v_fma_f32 v223, v223, v77, v227
	v_fmac_f32_e32 v138, v94, v224
	v_fmac_f32_e32 v139, v95, v225
	v_fmac_f32_e32 v222, v224, v74
	v_fmac_f32_e32 v223, v225, v75
	s_waitcnt lgkmcnt(0)
	v_fmac_f32_e32 v138, v106, v246
	v_fmac_f32_e32 v139, v107, v247
	v_fmac_f32_e32 v222, v246, v80
	v_fmac_f32_e32 v223, v247, v81
	v_fmac_f32_e32 v138, v104, v248
	v_fmac_f32_e32 v139, v105, v249
	v_fmac_f32_e32 v222, v248, v78
	v_fmac_f32_e32 v223, v249, v79
	v_fmac_f32_e32 v138, v114, v242
	v_fmac_f32_e32 v139, v115, v243
	v_fmac_f32_e32 v222, v242, v86
	v_fmac_f32_e32 v223, v243, v87
	v_fmac_f32_e32 v138, v110, v244
	v_fmac_f32_e32 v139, v111, v245
	v_fmac_f32_e32 v222, v244, v82
	v_fmac_f32_e32 v223, v245, v83
	v_fmac_f32_e32 v138, v120, v238
	v_fmac_f32_e32 v139, v121, v239
	v_fmac_f32_e32 v222, v238, v92
	v_fmac_f32_e32 v223, v239, v93
	v_fmac_f32_e32 v138, v118, v240
	v_fmac_f32_e32 v139, v119, v241
	v_fmac_f32_e32 v222, v240, v90
	v_fmac_f32_e32 v223, v241, v91
	v_fmac_f32_e32 v138, v124, v234
	v_fmac_f32_e32 v139, v125, v235
	v_fmac_f32_e32 v222, v234, v100
	v_fmac_f32_e32 v223, v235, v101
	v_fmac_f32_e32 v138, v122, v236
	v_fmac_f32_e32 v139, v123, v237
	v_fmac_f32_e32 v222, v236, v98
	v_fmac_f32_e32 v223, v237, v99
	v_fmac_f32_e32 v138, v130, v218
	v_fmac_f32_e32 v139, v131, v219
	v_fma_f32 v218, v218, v108, v222
	v_fma_f32 v219, v219, v109, v223
	v_fmac_f32_e32 v138, v126, v220
	v_fmac_f32_e32 v139, v127, v221
	v_fmac_f32_e32 v218, v220, v102
	v_fmac_f32_e32 v219, v221, v103
	v_fmac_f32_e32 v138, v134, v214
	v_fmac_f32_e32 v139, v135, v215
	v_fma_f32 v214, v214, v116, v218
	v_fma_f32 v215, v215, v117, v219
	ds_read_b128 v[218:221], v65 offset:16384
	v_fmac_f32_e32 v138, v132, v216
	v_fmac_f32_e32 v139, v133, v217
	v_fmac_f32_e32 v214, v216, v112
	v_fmac_f32_e32 v215, v217, v113
	v_add_f32_e32 v136, v136, v137
	v_add_f32_e32 v137, v138, v139
	v_add_f32_e32 v138, v214, v215
	ds_read_b128 v[214:217], v65 offset:17408
	s_waitcnt lgkmcnt(1)
	v_fma_f32 v222, v88, v218, 0
	v_fma_f32 v223, v89, v219, 0
	v_fma_f32 v218, v218, v72, 0
	v_fma_f32 v219, v219, v73, 0
	v_fmac_f32_e32 v222, v84, v220
	v_fmac_f32_e32 v223, v85, v221
	v_fma_f32 v224, v220, v70, v218
	v_fma_f32 v225, v221, v71, v219
	ds_read_b128 v[218:221], v65 offset:18432
	s_waitcnt lgkmcnt(1)
	v_fmac_f32_e32 v222, v96, v214
	v_fmac_f32_e32 v223, v97, v215
	v_fma_f32 v214, v214, v76, v224
	v_fma_f32 v215, v215, v77, v225
	v_fmac_f32_e32 v222, v94, v216
	v_fmac_f32_e32 v223, v95, v217
	v_fma_f32 v224, v216, v74, v214
	v_fma_f32 v225, v217, v75, v215
	ds_read_b128 v[214:217], v65 offset:19456
	s_waitcnt lgkmcnt(1)
	v_fmac_f32_e32 v222, v106, v218
	v_fmac_f32_e32 v223, v107, v219
	v_fma_f32 v218, v218, v80, v224
	v_fma_f32 v219, v219, v81, v225
	v_fmac_f32_e32 v222, v104, v220
	v_fmac_f32_e32 v223, v105, v221
	v_fma_f32 v224, v220, v78, v218
	v_fma_f32 v225, v221, v79, v219
	ds_read_b128 v[218:221], v65 offset:20480
	s_waitcnt lgkmcnt(1)
	v_fmac_f32_e32 v222, v114, v214
	v_fmac_f32_e32 v223, v115, v215
	v_fma_f32 v214, v214, v86, v224
	v_fma_f32 v215, v215, v87, v225
	v_fmac_f32_e32 v222, v110, v216
	v_fmac_f32_e32 v223, v111, v217
	v_fma_f32 v224, v216, v82, v214
	v_fma_f32 v225, v217, v83, v215
	ds_read_b128 v[214:217], v65 offset:21504
	s_waitcnt lgkmcnt(1)
	v_fmac_f32_e32 v222, v120, v218
	v_fmac_f32_e32 v223, v121, v219
	v_fma_f32 v218, v218, v92, v224
	v_fma_f32 v219, v219, v93, v225
	v_fmac_f32_e32 v222, v118, v220
	v_fmac_f32_e32 v223, v119, v221
	v_fma_f32 v224, v220, v90, v218
	v_fma_f32 v225, v221, v91, v219
	ds_read_b128 v[218:221], v65 offset:22528
	s_waitcnt lgkmcnt(1)
	v_fmac_f32_e32 v222, v124, v214
	v_fmac_f32_e32 v223, v125, v215
	v_fma_f32 v214, v214, v100, v224
	v_fma_f32 v215, v215, v101, v225
	v_fmac_f32_e32 v222, v122, v216
	v_fmac_f32_e32 v223, v123, v217
	v_fma_f32 v224, v216, v98, v214
	v_fma_f32 v225, v217, v99, v215
	ds_read_b128 v[214:217], v65 offset:23552
	s_waitcnt lgkmcnt(1)
	v_fmac_f32_e32 v222, v130, v218
	v_fmac_f32_e32 v223, v131, v219
	v_fma_f32 v218, v218, v108, v224
	v_fma_f32 v219, v219, v109, v225
	v_fmac_f32_e32 v222, v126, v220
	v_fmac_f32_e32 v223, v127, v221
	v_fmac_f32_e32 v218, v220, v102
	v_fmac_f32_e32 v219, v221, v103
	s_waitcnt lgkmcnt(0)
	v_fma_f32 v220, v134, v214, v222
	v_fma_f32 v221, v135, v215, v223
	v_fma_f32 v214, v214, v116, v218
	v_fma_f32 v215, v215, v117, v219
	v_fmac_f32_e32 v220, v132, v216
	v_fmac_f32_e32 v221, v133, v217
	v_fmac_f32_e32 v214, v216, v112
	v_fmac_f32_e32 v215, v217, v113
	v_add_f32_e32 v139, v220, v221
	v_add_f32_e32 v213, v214, v215
	ds_read_b128 v[214:217], v65 offset:31744
	ds_read_b128 v[218:221], v65 offset:30720
	ds_read_b128 v[222:225], v65 offset:25600
	ds_read_b128 v[226:229], v65 offset:24576
	ds_read_b128 v[234:237], v65 offset:29696
	ds_read_b128 v[238:241], v65 offset:28672
	ds_read_b128 v[242:245], v65 offset:27648
	ds_read_b128 v[246:249], v65 offset:26624
	s_waitcnt lgkmcnt(4)
	v_fma_f32 v196, v88, v226, 0
	v_fma_f32 v197, v89, v227, 0
	v_fma_f32 v226, v226, v72, 0
	v_fma_f32 v227, v227, v73, 0
	v_fmac_f32_e32 v196, v84, v228
	v_fmac_f32_e32 v197, v85, v229
	v_fmac_f32_e32 v226, v228, v70
	v_fmac_f32_e32 v227, v229, v71
	v_fmac_f32_e32 v196, v96, v222
	v_fmac_f32_e32 v197, v97, v223
	v_fma_f32 v222, v222, v76, v226
	v_fma_f32 v223, v223, v77, v227
	v_fmac_f32_e32 v196, v94, v224
	v_fmac_f32_e32 v197, v95, v225
	v_fmac_f32_e32 v222, v224, v74
	v_fmac_f32_e32 v223, v225, v75
	s_waitcnt lgkmcnt(0)
	v_fmac_f32_e32 v196, v106, v246
	v_fmac_f32_e32 v197, v107, v247
	v_fmac_f32_e32 v222, v246, v80
	v_fmac_f32_e32 v223, v247, v81
	v_fmac_f32_e32 v196, v104, v248
	v_fmac_f32_e32 v197, v105, v249
	v_fmac_f32_e32 v222, v248, v78
	v_fmac_f32_e32 v223, v249, v79
	v_fmac_f32_e32 v196, v114, v242
	v_fmac_f32_e32 v197, v115, v243
	v_fmac_f32_e32 v222, v242, v86
	v_fmac_f32_e32 v223, v243, v87
	v_fmac_f32_e32 v196, v110, v244
	v_fmac_f32_e32 v197, v111, v245
	v_fmac_f32_e32 v222, v244, v82
	v_fmac_f32_e32 v223, v245, v83
	v_fmac_f32_e32 v196, v120, v238
	v_fmac_f32_e32 v197, v121, v239
	v_fmac_f32_e32 v222, v238, v92
	v_fmac_f32_e32 v223, v239, v93
	v_fmac_f32_e32 v196, v118, v240
	v_fmac_f32_e32 v197, v119, v241
	v_fmac_f32_e32 v222, v240, v90
	v_fmac_f32_e32 v223, v241, v91
	v_fmac_f32_e32 v196, v124, v234
	v_fmac_f32_e32 v197, v125, v235
	v_fmac_f32_e32 v222, v234, v100
	v_fmac_f32_e32 v223, v235, v101
	v_fmac_f32_e32 v196, v122, v236
	v_fmac_f32_e32 v197, v123, v237
	v_fmac_f32_e32 v222, v236, v98
	v_fmac_f32_e32 v223, v237, v99
	v_fmac_f32_e32 v196, v130, v218
	v_fmac_f32_e32 v197, v131, v219
	v_fma_f32 v218, v218, v108, v222
	v_fma_f32 v219, v219, v109, v223
	v_fmac_f32_e32 v196, v126, v220
	v_fmac_f32_e32 v197, v127, v221
	v_fmac_f32_e32 v218, v220, v102
	v_fmac_f32_e32 v219, v221, v103
	v_fmac_f32_e32 v196, v134, v214
	v_fmac_f32_e32 v197, v135, v215
	v_fma_f32 v214, v214, v116, v218
	v_fma_f32 v215, v215, v117, v219
	ds_read_b128 v[218:221], v65 offset:32768
	ds_read_b128 v[222:225], v65 offset:33792
	v_fmac_f32_e32 v196, v132, v216
	v_fmac_f32_e32 v197, v133, v217
	v_fma_f32 v216, v216, v112, v214
	v_fma_f32 v217, v217, v113, v215
	v_add_f32_e32 v214, v196, v197
	v_add_f32_e32 v215, v216, v217
	s_waitcnt lgkmcnt(1)
	v_fma_f32 v196, v88, v218, 0
	v_fma_f32 v197, v89, v219, 0
	v_fma_f32 v216, v218, v72, 0
	v_fma_f32 v217, v219, v73, 0
	v_fmac_f32_e32 v196, v84, v220
	v_fmac_f32_e32 v197, v85, v221
	v_fma_f32 v220, v220, v70, v216
	v_fma_f32 v221, v221, v71, v217
	ds_read_b128 v[216:219], v65 offset:34816
	s_waitcnt lgkmcnt(1)
	v_fmac_f32_e32 v196, v96, v222
	v_fmac_f32_e32 v197, v97, v223
	v_fmac_f32_e32 v220, v222, v76
	v_fmac_f32_e32 v221, v223, v77
	v_fmac_f32_e32 v196, v94, v224
	v_fmac_f32_e32 v197, v95, v225
	v_fma_f32 v224, v224, v74, v220
	v_fma_f32 v225, v225, v75, v221
	ds_read_b128 v[220:223], v65 offset:35840
	s_waitcnt lgkmcnt(1)
	v_fmac_f32_e32 v196, v106, v216
	v_fmac_f32_e32 v197, v107, v217
	v_fma_f32 v216, v216, v80, v224
	v_fma_f32 v217, v217, v81, v225
	v_fmac_f32_e32 v196, v104, v218
	v_fmac_f32_e32 v197, v105, v219
	v_fma_f32 v224, v218, v78, v216
	v_fma_f32 v225, v219, v79, v217
	ds_read_b128 v[216:219], v65 offset:36864
	s_waitcnt lgkmcnt(1)
	v_fmac_f32_e32 v196, v114, v220
	v_fmac_f32_e32 v197, v115, v221
	v_fma_f32 v220, v220, v86, v224
	v_fma_f32 v221, v221, v87, v225
	v_fmac_f32_e32 v196, v110, v222
	v_fmac_f32_e32 v197, v111, v223
	v_fma_f32 v224, v222, v82, v220
	v_fma_f32 v225, v223, v83, v221
	ds_read_b128 v[220:223], v65 offset:37888
	s_waitcnt lgkmcnt(1)
	v_fmac_f32_e32 v196, v120, v216
	v_fmac_f32_e32 v197, v121, v217
	v_fma_f32 v216, v216, v92, v224
	v_fma_f32 v217, v217, v93, v225
	v_fmac_f32_e32 v196, v118, v218
	v_fmac_f32_e32 v197, v119, v219
	v_fma_f32 v224, v218, v90, v216
	v_fma_f32 v225, v219, v91, v217
	ds_read_b128 v[216:219], v65 offset:38912
	s_waitcnt lgkmcnt(1)
	v_fmac_f32_e32 v196, v124, v220
	v_fmac_f32_e32 v197, v125, v221
	v_fma_f32 v220, v220, v100, v224
	v_fma_f32 v221, v221, v101, v225
	v_fmac_f32_e32 v196, v122, v222
	v_fmac_f32_e32 v197, v123, v223
	v_fma_f32 v224, v222, v98, v220
	v_fma_f32 v225, v223, v99, v221
	ds_read_b128 v[220:223], v65 offset:39936
	s_waitcnt lgkmcnt(1)
	v_fmac_f32_e32 v196, v130, v216
	v_fmac_f32_e32 v197, v131, v217
	v_fma_f32 v216, v216, v108, v224
	v_fma_f32 v217, v217, v109, v225
	v_fmac_f32_e32 v196, v126, v218
	v_fmac_f32_e32 v197, v127, v219
	v_fmac_f32_e32 v216, v218, v102
	v_fmac_f32_e32 v217, v219, v103
	s_waitcnt lgkmcnt(0)
	v_fmac_f32_e32 v196, v134, v220
	v_fmac_f32_e32 v197, v135, v221
	v_fmac_f32_e32 v216, v220, v116
	v_fmac_f32_e32 v217, v221, v117
	v_fmac_f32_e32 v196, v132, v222
	v_fmac_f32_e32 v197, v133, v223
	v_fma_f32 v218, v222, v112, v216
	v_fma_f32 v219, v223, v113, v217
	v_add_f32_e32 v216, v196, v197
	v_add_f32_e32 v217, v218, v219
	ds_read_b128 v[218:221], v65 offset:48128
	ds_read_b128 v[222:225], v65 offset:47104
	ds_read_b128 v[226:229], v65 offset:40960
	ds_read_b128 v[234:237], v65 offset:41984
	ds_read_b128 v[238:241], v65 offset:46080
	ds_read_b128 v[242:245], v65 offset:45056
	ds_read_b128 v[246:249], v65 offset:44032
	s_waitcnt lgkmcnt(4)
	v_fma_f32 v196, v88, v226, 0
	v_fma_f32 v197, v89, v227, 0
	v_fma_f32 v226, v226, v72, 0
	v_fma_f32 v227, v227, v73, 0
	v_fmac_f32_e32 v196, v84, v228
	v_fmac_f32_e32 v197, v85, v229
	v_fma_f32 v194, v228, v70, v226
	v_fma_f32 v195, v229, v71, v227
	ds_read_b128 v[226:229], v65 offset:43008
	s_waitcnt lgkmcnt(4)
	v_fmac_f32_e32 v196, v96, v234
	v_fmac_f32_e32 v197, v97, v235
	v_fmac_f32_e32 v194, v234, v76
	v_fmac_f32_e32 v195, v235, v77
	v_fmac_f32_e32 v196, v94, v236
	v_fmac_f32_e32 v197, v95, v237
	v_fmac_f32_e32 v194, v236, v74
	v_fmac_f32_e32 v195, v237, v75
	s_waitcnt lgkmcnt(0)
	v_fmac_f32_e32 v196, v106, v226
	v_fmac_f32_e32 v197, v107, v227
	v_fmac_f32_e32 v194, v226, v80
	v_fmac_f32_e32 v195, v227, v81
	v_fmac_f32_e32 v196, v104, v228
	v_fmac_f32_e32 v197, v105, v229
	v_fmac_f32_e32 v194, v228, v78
	v_fmac_f32_e32 v195, v229, v79
	v_fmac_f32_e32 v196, v114, v246
	v_fmac_f32_e32 v197, v115, v247
	v_fmac_f32_e32 v194, v246, v86
	v_fmac_f32_e32 v195, v247, v87
	v_fmac_f32_e32 v196, v110, v248
	v_fmac_f32_e32 v197, v111, v249
	v_fmac_f32_e32 v194, v248, v82
	v_fmac_f32_e32 v195, v249, v83
	v_fmac_f32_e32 v196, v120, v242
	v_fmac_f32_e32 v197, v121, v243
	v_fmac_f32_e32 v194, v242, v92
	v_fmac_f32_e32 v195, v243, v93
	v_fmac_f32_e32 v196, v118, v244
	v_fmac_f32_e32 v197, v119, v245
	v_fmac_f32_e32 v194, v244, v90
	v_fmac_f32_e32 v195, v245, v91
	v_fmac_f32_e32 v196, v124, v238
	v_fmac_f32_e32 v197, v125, v239
	v_fmac_f32_e32 v194, v238, v100
	v_fmac_f32_e32 v195, v239, v101
	v_fmac_f32_e32 v196, v122, v240
	v_fmac_f32_e32 v197, v123, v241
	v_fmac_f32_e32 v194, v240, v98
	v_fmac_f32_e32 v195, v241, v99
	v_fmac_f32_e32 v196, v130, v222
	v_fmac_f32_e32 v197, v131, v223
	v_fmac_f32_e32 v194, v222, v108
	v_fmac_f32_e32 v195, v223, v109
	v_fmac_f32_e32 v196, v126, v224
	v_fmac_f32_e32 v197, v127, v225
	v_fmac_f32_e32 v194, v224, v102
	v_fmac_f32_e32 v195, v225, v103
	ds_read_b128 v[222:225], v65 offset:49152
	ds_read_b128 v[226:229], v65 offset:50176
	v_fmac_f32_e32 v196, v134, v218
	v_fmac_f32_e32 v197, v135, v219
	v_fmac_f32_e32 v194, v218, v116
	v_fmac_f32_e32 v195, v219, v117
	v_fmac_f32_e32 v196, v132, v220
	v_fmac_f32_e32 v197, v133, v221
	v_fmac_f32_e32 v194, v220, v112
	v_fmac_f32_e32 v195, v221, v113
	v_add_f32_e32 v218, v196, v197
	v_add_f32_e32 v219, v194, v195
	s_waitcnt lgkmcnt(1)
	v_fma_f32 v194, v88, v222, 0
	v_fma_f32 v195, v89, v223, 0
	v_fma_f32 v196, v222, v72, 0
	v_fma_f32 v197, v223, v73, 0
	ds_read_b128 v[220:223], v65 offset:51200
	v_fmac_f32_e32 v194, v84, v224
	v_fmac_f32_e32 v195, v85, v225
	v_fmac_f32_e32 v196, v224, v70
	v_fmac_f32_e32 v197, v225, v71
	s_waitcnt lgkmcnt(1)
	v_fmac_f32_e32 v194, v96, v226
	v_fmac_f32_e32 v195, v97, v227
	v_fmac_f32_e32 v196, v226, v76
	v_fmac_f32_e32 v197, v227, v77
	ds_read_b128 v[224:227], v65 offset:52224
	v_fmac_f32_e32 v194, v94, v228
	v_fmac_f32_e32 v195, v95, v229
	v_fmac_f32_e32 v196, v228, v74
	v_fmac_f32_e32 v197, v229, v75
	s_waitcnt lgkmcnt(1)
	v_fmac_f32_e32 v194, v106, v220
	v_fmac_f32_e32 v195, v107, v221
	v_fmac_f32_e32 v196, v220, v80
	v_fmac_f32_e32 v197, v221, v81
	v_fmac_f32_e32 v194, v104, v222
	v_fmac_f32_e32 v195, v105, v223
	v_fmac_f32_e32 v196, v222, v78
	v_fmac_f32_e32 v197, v223, v79
	ds_read_b128 v[220:223], v65 offset:53248
	s_waitcnt lgkmcnt(1)
	v_fmac_f32_e32 v194, v114, v224
	v_fmac_f32_e32 v195, v115, v225
	v_fmac_f32_e32 v196, v224, v86
	v_fmac_f32_e32 v197, v225, v87
	v_fmac_f32_e32 v194, v110, v226
	v_fmac_f32_e32 v195, v111, v227
	v_fmac_f32_e32 v196, v226, v82
	v_fmac_f32_e32 v197, v227, v83
	ds_read_b128 v[224:227], v65 offset:54272
	s_waitcnt lgkmcnt(1)
	v_fmac_f32_e32 v194, v120, v220
	v_fmac_f32_e32 v195, v121, v221
	v_fmac_f32_e32 v196, v220, v92
	v_fmac_f32_e32 v197, v221, v93
	v_fmac_f32_e32 v194, v118, v222
	v_fmac_f32_e32 v195, v119, v223
	v_fmac_f32_e32 v196, v222, v90
	v_fmac_f32_e32 v197, v223, v91
	ds_read_b128 v[220:223], v65 offset:55296
	s_waitcnt lgkmcnt(1)
	v_fmac_f32_e32 v194, v124, v224
	v_fmac_f32_e32 v195, v125, v225
	v_fmac_f32_e32 v196, v224, v100
	v_fmac_f32_e32 v197, v225, v101
	v_fmac_f32_e32 v194, v122, v226
	v_fmac_f32_e32 v195, v123, v227
	v_fmac_f32_e32 v196, v226, v98
	v_fmac_f32_e32 v197, v227, v99
	ds_read_b128 v[224:227], v65 offset:56320
	s_waitcnt lgkmcnt(1)
	v_fmac_f32_e32 v194, v130, v220
	v_fmac_f32_e32 v195, v131, v221
	v_fmac_f32_e32 v196, v220, v108
	v_fmac_f32_e32 v197, v221, v109
	v_fmac_f32_e32 v194, v126, v222
	v_fmac_f32_e32 v195, v127, v223
	v_fmac_f32_e32 v196, v222, v102
	v_fmac_f32_e32 v197, v223, v103
	s_waitcnt lgkmcnt(0)
	v_fmac_f32_e32 v194, v134, v224
	v_fmac_f32_e32 v195, v135, v225
	v_fmac_f32_e32 v196, v224, v116
	v_fmac_f32_e32 v197, v225, v117
	v_fmac_f32_e32 v194, v132, v226
	v_fmac_f32_e32 v195, v133, v227
	v_fmac_f32_e32 v196, v226, v112
	v_fmac_f32_e32 v197, v227, v113
	ds_read_b128 v[222:225], v65 offset:64512
	ds_read_b128 v[226:229], v65 offset:57344
	ds_read_b128 v[234:237], v65 offset:63488
	ds_read_b128 v[238:241], v65 offset:58368
	ds_read_b128 v[242:245], v65 offset:62464
	ds_read_b128 v[246:249], v65 offset:61440
	v_add_f32_e32 v220, v194, v195
	v_add_f32_e32 v221, v196, v197
	s_waitcnt lgkmcnt(4)
	v_fma_f32 v194, v88, v226, 0
	v_fma_f32 v195, v89, v227, 0
	v_fma_f32 v196, v226, v72, 0
	v_fma_f32 v197, v227, v73, 0
	v_fmac_f32_e32 v194, v84, v228
	v_fmac_f32_e32 v195, v85, v229
	v_fmac_f32_e32 v196, v228, v70
	v_fmac_f32_e32 v197, v229, v71
	ds_read_b128 v[226:229], v65 offset:59392
	s_waitcnt lgkmcnt(3)
	v_fmac_f32_e32 v194, v96, v238
	v_fmac_f32_e32 v195, v97, v239
	v_fmac_f32_e32 v196, v238, v76
	v_fmac_f32_e32 v197, v239, v77
	v_fmac_f32_e32 v194, v94, v240
	v_fmac_f32_e32 v195, v95, v241
	v_fmac_f32_e32 v196, v240, v74
	v_fmac_f32_e32 v197, v241, v75
	ds_read_b128 v[238:241], v65 offset:60416
	s_waitcnt lgkmcnt(1)
	v_fmac_f32_e32 v194, v106, v226
	v_fmac_f32_e32 v195, v107, v227
	v_fmac_f32_e32 v196, v226, v80
	v_fmac_f32_e32 v197, v227, v81
	v_fmac_f32_e32 v194, v104, v228
	v_fmac_f32_e32 v195, v105, v229
	v_fmac_f32_e32 v196, v228, v78
	v_fmac_f32_e32 v197, v229, v79
	s_waitcnt lgkmcnt(0)
	v_fmac_f32_e32 v194, v114, v238
	v_fmac_f32_e32 v195, v115, v239
	v_fmac_f32_e32 v196, v238, v86
	v_fmac_f32_e32 v197, v239, v87
	v_fmac_f32_e32 v194, v110, v240
	v_fmac_f32_e32 v195, v111, v241
	v_fmac_f32_e32 v196, v240, v82
	v_fmac_f32_e32 v197, v241, v83
	v_fmac_f32_e32 v194, v120, v246
	v_fmac_f32_e32 v195, v121, v247
	v_fmac_f32_e32 v196, v246, v92
	v_fmac_f32_e32 v197, v247, v93
	v_fmac_f32_e32 v194, v118, v248
	v_fmac_f32_e32 v195, v119, v249
	v_fmac_f32_e32 v196, v248, v90
	v_fmac_f32_e32 v197, v249, v91
	v_fmac_f32_e32 v194, v124, v242
	v_fmac_f32_e32 v195, v125, v243
	v_fmac_f32_e32 v196, v242, v100
	v_fmac_f32_e32 v197, v243, v101
	v_fmac_f32_e32 v194, v122, v244
	v_fmac_f32_e32 v195, v123, v245
	v_fmac_f32_e32 v196, v244, v98
	v_fmac_f32_e32 v197, v245, v99
	v_fmac_f32_e32 v194, v130, v234
	v_fmac_f32_e32 v195, v131, v235
	v_fmac_f32_e32 v196, v234, v108
	v_fmac_f32_e32 v197, v235, v109
	v_fmac_f32_e32 v194, v126, v236
	v_fmac_f32_e32 v195, v127, v237
	v_fmac_f32_e32 v196, v236, v102
	v_fmac_f32_e32 v197, v237, v103
	v_fmac_f32_e32 v194, v134, v222
	v_fmac_f32_e32 v195, v135, v223
	v_fmac_f32_e32 v196, v222, v116
	v_fmac_f32_e32 v197, v223, v117
	v_add_u32_e32 v222, 0x10000, v65
	v_fmac_f32_e32 v194, v132, v224
	v_fmac_f32_e32 v195, v133, v225
	ds_read_b128 v[226:229], v222
	v_add_f32_e32 v222, v194, v195
	v_add_u32_e32 v194, 0x10400, v65
	ds_read_b128 v[234:237], v194
	v_fmac_f32_e32 v196, v224, v112
	v_fmac_f32_e32 v197, v225, v113
	s_waitcnt lgkmcnt(1)
	v_fma_f32 v194, v88, v226, 0
	v_fma_f32 v195, v89, v227, 0
	v_add_f32_e32 v223, v196, v197
	v_fma_f32 v196, v226, v72, 0
	v_fma_f32 v197, v227, v73, 0
	v_add_u32_e32 v224, 0x10800, v65
	v_fmac_f32_e32 v194, v84, v228
	v_fmac_f32_e32 v195, v85, v229
	v_fmac_f32_e32 v196, v228, v70
	v_fmac_f32_e32 v197, v229, v71
	ds_read_b128 v[224:227], v224
	s_waitcnt lgkmcnt(1)
	v_fmac_f32_e32 v194, v96, v234
	v_fmac_f32_e32 v195, v97, v235
	v_fmac_f32_e32 v196, v234, v76
	v_fmac_f32_e32 v197, v235, v77
	v_add_u32_e32 v228, 0x10c00, v65
	v_fmac_f32_e32 v194, v94, v236
	v_fmac_f32_e32 v195, v95, v237
	v_fmac_f32_e32 v196, v236, v74
	v_fmac_f32_e32 v197, v237, v75
	ds_read_b128 v[234:237], v228
	s_waitcnt lgkmcnt(1)
	v_fmac_f32_e32 v194, v106, v224
	v_fmac_f32_e32 v195, v107, v225
	v_fmac_f32_e32 v196, v224, v80
	v_fmac_f32_e32 v197, v225, v81
	v_add_u32_e32 v224, 0x11000, v65
	v_fmac_f32_e32 v194, v104, v226
	v_fmac_f32_e32 v195, v105, v227
	v_fmac_f32_e32 v196, v226, v78
	v_fmac_f32_e32 v197, v227, v79
	ds_read_b128 v[224:227], v224
	s_waitcnt lgkmcnt(1)
	v_fmac_f32_e32 v194, v114, v234
	v_fmac_f32_e32 v195, v115, v235
	v_fmac_f32_e32 v196, v234, v86
	v_fmac_f32_e32 v197, v235, v87
	v_add_u32_e32 v228, 0x11400, v65
	v_fmac_f32_e32 v194, v110, v236
	v_fmac_f32_e32 v195, v111, v237
	v_fmac_f32_e32 v196, v236, v82
	v_fmac_f32_e32 v197, v237, v83
	ds_read_b128 v[234:237], v228
	s_waitcnt lgkmcnt(1)
	v_fmac_f32_e32 v194, v120, v224
	v_fmac_f32_e32 v195, v121, v225
	v_fmac_f32_e32 v196, v224, v92
	v_fmac_f32_e32 v197, v225, v93
	v_add_u32_e32 v224, 0x11800, v65
	v_fmac_f32_e32 v194, v118, v226
	v_fmac_f32_e32 v195, v119, v227
	v_fmac_f32_e32 v196, v226, v90
	v_fmac_f32_e32 v197, v227, v91
	ds_read_b128 v[224:227], v224
	s_waitcnt lgkmcnt(1)
	v_fmac_f32_e32 v194, v124, v234
	v_fmac_f32_e32 v195, v125, v235
	v_fmac_f32_e32 v196, v234, v100
	v_fmac_f32_e32 v197, v235, v101
	v_add_u32_e32 v228, 0x11c00, v65
	v_fmac_f32_e32 v194, v122, v236
	v_fmac_f32_e32 v195, v123, v237
	v_fmac_f32_e32 v196, v236, v98
	v_fmac_f32_e32 v197, v237, v99
	ds_read_b128 v[234:237], v228
	s_waitcnt lgkmcnt(1)
	v_fmac_f32_e32 v194, v130, v224
	v_fmac_f32_e32 v195, v131, v225
	v_fmac_f32_e32 v196, v224, v108
	v_fmac_f32_e32 v197, v225, v109
	v_fmac_f32_e32 v194, v126, v226
	v_fmac_f32_e32 v195, v127, v227
	v_fmac_f32_e32 v196, v226, v102
	v_fmac_f32_e32 v197, v227, v103
	ds_read_b128 v[226:229], v145
	s_waitcnt lgkmcnt(1)
	v_fmac_f32_e32 v194, v134, v234
	v_fmac_f32_e32 v195, v135, v235
	v_fmac_f32_e32 v196, v234, v116
	v_fmac_f32_e32 v197, v235, v117
	v_fmac_f32_e32 v194, v132, v236
	v_fmac_f32_e32 v195, v133, v237
	v_fmac_f32_e32 v196, v236, v112
	v_fmac_f32_e32 v197, v237, v113
	v_add_f32_e32 v224, v194, v195
	v_add_u32_e32 v194, 0x13c00, v65
	ds_read_b128 v[234:237], v194
	ds_read_b128 v[238:241], v146
	ds_read_b128 v[242:245], v147
	ds_read_b128 v[246:249], v151
	v_add_f32_e32 v225, v196, v197
	s_waitcnt lgkmcnt(4)
	v_fma_f32 v194, v88, v226, 0
	v_fma_f32 v195, v89, v227, 0
	v_fma_f32 v196, v226, v72, 0
	v_fma_f32 v197, v227, v73, 0
	v_fmac_f32_e32 v194, v84, v228
	v_fmac_f32_e32 v195, v85, v229
	v_fmac_f32_e32 v196, v228, v70
	v_fmac_f32_e32 v197, v229, v71
	ds_read_b128 v[226:229], v150
	s_waitcnt lgkmcnt(1)
	v_fmac_f32_e32 v194, v96, v246
	v_fmac_f32_e32 v195, v97, v247
	v_fmac_f32_e32 v196, v246, v76
	v_fmac_f32_e32 v197, v247, v77
	v_fmac_f32_e32 v194, v94, v248
	v_fmac_f32_e32 v195, v95, v249
	v_fmac_f32_e32 v196, v248, v74
	v_fmac_f32_e32 v197, v249, v75
	ds_read_b128 v[246:249], v149
	s_waitcnt lgkmcnt(1)
	v_fmac_f32_e32 v194, v106, v226
	v_fmac_f32_e32 v195, v107, v227
	v_fmac_f32_e32 v196, v226, v80
	v_fmac_f32_e32 v197, v227, v81
	v_fmac_f32_e32 v194, v104, v228
	v_fmac_f32_e32 v195, v105, v229
	v_fmac_f32_e32 v196, v228, v78
	v_fmac_f32_e32 v197, v229, v79
	ds_read_b128 v[226:229], v148
	s_waitcnt lgkmcnt(1)
	v_fmac_f32_e32 v194, v114, v246
	v_fmac_f32_e32 v195, v115, v247
	v_fmac_f32_e32 v196, v246, v86
	v_fmac_f32_e32 v197, v247, v87
	v_fmac_f32_e32 v194, v110, v248
	v_fmac_f32_e32 v195, v111, v249
	v_fmac_f32_e32 v196, v248, v82
	v_fmac_f32_e32 v197, v249, v83
	s_waitcnt lgkmcnt(0)
	v_fmac_f32_e32 v194, v120, v226
	v_fmac_f32_e32 v195, v121, v227
	v_fmac_f32_e32 v196, v226, v92
	v_fmac_f32_e32 v197, v227, v93
	v_fmac_f32_e32 v194, v118, v228
	v_fmac_f32_e32 v195, v119, v229
	v_fmac_f32_e32 v196, v228, v90
	v_fmac_f32_e32 v197, v229, v91
	v_fmac_f32_e32 v194, v124, v242
	v_fmac_f32_e32 v195, v125, v243
	v_fmac_f32_e32 v196, v242, v100
	v_fmac_f32_e32 v197, v243, v101
	v_fmac_f32_e32 v194, v122, v244
	v_fmac_f32_e32 v195, v123, v245
	v_fmac_f32_e32 v196, v244, v98
	v_fmac_f32_e32 v197, v245, v99
	v_fmac_f32_e32 v194, v130, v238
	v_fmac_f32_e32 v195, v131, v239
	v_fmac_f32_e32 v196, v238, v108
	v_fmac_f32_e32 v197, v239, v109
	v_fmac_f32_e32 v194, v126, v240
	v_fmac_f32_e32 v195, v127, v241
	v_fmac_f32_e32 v196, v240, v102
	v_fmac_f32_e32 v197, v241, v103
	ds_read_b128 v[238:241], v152
	v_fmac_f32_e32 v194, v134, v234
	v_fmac_f32_e32 v195, v135, v235
	v_fmac_f32_e32 v196, v234, v116
	v_fmac_f32_e32 v197, v235, v117
	v_fmac_f32_e32 v194, v132, v236
	v_fmac_f32_e32 v195, v133, v237
	v_fmac_f32_e32 v196, v236, v112
	v_fmac_f32_e32 v197, v237, v113
	ds_read_b128 v[234:237], v153
	v_add_f32_e32 v226, v194, v195
	v_add_f32_e32 v227, v196, v197
	s_waitcnt lgkmcnt(1)
	v_fma_f32 v194, v88, v238, 0
	v_fma_f32 v195, v89, v239, 0
	v_fma_f32 v196, v238, v72, 0
	v_fma_f32 v197, v239, v73, 0
	v_fmac_f32_e32 v194, v84, v240
	v_fmac_f32_e32 v195, v85, v241
	v_fmac_f32_e32 v196, v240, v70
	v_fmac_f32_e32 v197, v241, v71
	ds_read_b128 v[238:241], v154
	s_waitcnt lgkmcnt(1)
	v_fmac_f32_e32 v194, v96, v234
	v_fmac_f32_e32 v195, v97, v235
	v_fmac_f32_e32 v196, v234, v76
	v_fmac_f32_e32 v197, v235, v77
	v_fmac_f32_e32 v194, v94, v236
	v_fmac_f32_e32 v195, v95, v237
	v_fmac_f32_e32 v196, v236, v74
	v_fmac_f32_e32 v197, v237, v75
	ds_read_b128 v[234:237], v155
	s_waitcnt lgkmcnt(1)
	v_fmac_f32_e32 v194, v106, v238
	v_fmac_f32_e32 v195, v107, v239
	v_fmac_f32_e32 v196, v238, v80
	v_fmac_f32_e32 v197, v239, v81
	v_fmac_f32_e32 v194, v104, v240
	v_fmac_f32_e32 v195, v105, v241
	v_fmac_f32_e32 v196, v240, v78
	v_fmac_f32_e32 v197, v241, v79
	ds_read_b128 v[238:241], v156
	s_waitcnt lgkmcnt(1)
	v_fmac_f32_e32 v194, v114, v234
	v_fmac_f32_e32 v195, v115, v235
	v_fmac_f32_e32 v196, v234, v86
	v_fmac_f32_e32 v197, v235, v87
	v_fmac_f32_e32 v194, v110, v236
	v_fmac_f32_e32 v195, v111, v237
	v_fmac_f32_e32 v196, v236, v82
	v_fmac_f32_e32 v197, v237, v83
	ds_read_b128 v[234:237], v157
	s_waitcnt lgkmcnt(1)
	v_fmac_f32_e32 v194, v120, v238
	v_fmac_f32_e32 v195, v121, v239
	v_fmac_f32_e32 v196, v238, v92
	v_fmac_f32_e32 v197, v239, v93
	v_fmac_f32_e32 v194, v118, v240
	v_fmac_f32_e32 v195, v119, v241
	v_fmac_f32_e32 v196, v240, v90
	v_fmac_f32_e32 v197, v241, v91
	ds_read_b128 v[238:241], v158
	s_waitcnt lgkmcnt(1)
	v_fmac_f32_e32 v194, v124, v234
	v_fmac_f32_e32 v195, v125, v235
	v_fmac_f32_e32 v196, v234, v100
	v_fmac_f32_e32 v197, v235, v101
	v_fmac_f32_e32 v194, v122, v236
	v_fmac_f32_e32 v195, v123, v237
	v_fmac_f32_e32 v196, v236, v98
	v_fmac_f32_e32 v197, v237, v99
	ds_read_b128 v[234:237], v159
	s_waitcnt lgkmcnt(1)
	v_fmac_f32_e32 v194, v130, v238
	v_fmac_f32_e32 v195, v131, v239
	v_fmac_f32_e32 v196, v238, v108
	v_fmac_f32_e32 v197, v239, v109
	v_fmac_f32_e32 v194, v126, v240
	v_fmac_f32_e32 v195, v127, v241
	v_fmac_f32_e32 v196, v240, v102
	v_fmac_f32_e32 v197, v241, v103
	s_waitcnt lgkmcnt(0)
	v_fmac_f32_e32 v194, v134, v234
	v_fmac_f32_e32 v195, v135, v235
	v_fmac_f32_e32 v196, v234, v116
	v_fmac_f32_e32 v197, v235, v117
	v_fmac_f32_e32 v194, v132, v236
	v_fmac_f32_e32 v195, v133, v237
	v_fmac_f32_e32 v196, v236, v112
	v_fmac_f32_e32 v197, v237, v113
	ds_read_b128 v[234:237], v161
	ds_read_b128 v[238:241], v160
	ds_read_b128 v[242:245], v162
	ds_read_b128 v[246:249], v167
	v_add_f32_e32 v228, v194, v195
	v_add_f32_e32 v229, v196, v197
	s_waitcnt lgkmcnt(3)
	v_fma_f32 v194, v88, v234, 0
	v_fma_f32 v195, v89, v235, 0
	v_fma_f32 v196, v234, v72, 0
	v_fma_f32 v197, v235, v73, 0
	v_fmac_f32_e32 v194, v84, v236
	v_fmac_f32_e32 v195, v85, v237
	v_fmac_f32_e32 v196, v236, v70
	v_fmac_f32_e32 v197, v237, v71
	ds_read_b128 v[234:237], v166
	s_waitcnt lgkmcnt(1)
	v_fmac_f32_e32 v194, v96, v246
	v_fmac_f32_e32 v195, v97, v247
	v_fmac_f32_e32 v196, v246, v76
	v_fmac_f32_e32 v197, v247, v77
	v_fmac_f32_e32 v194, v94, v248
	v_fmac_f32_e32 v195, v95, v249
	v_fmac_f32_e32 v196, v248, v74
	v_fmac_f32_e32 v197, v249, v75
	ds_read_b128 v[246:249], v165
	s_waitcnt lgkmcnt(1)
	v_fmac_f32_e32 v194, v106, v234
	v_fmac_f32_e32 v195, v107, v235
	v_fmac_f32_e32 v196, v234, v80
	v_fmac_f32_e32 v197, v235, v81
	v_fmac_f32_e32 v194, v104, v236
	v_fmac_f32_e32 v195, v105, v237
	v_fmac_f32_e32 v196, v236, v78
	v_fmac_f32_e32 v197, v237, v79
	ds_read_b128 v[234:237], v164
	s_waitcnt lgkmcnt(1)
	v_fmac_f32_e32 v194, v114, v246
	v_fmac_f32_e32 v195, v115, v247
	v_fmac_f32_e32 v196, v246, v86
	v_fmac_f32_e32 v197, v247, v87
	v_fmac_f32_e32 v194, v110, v248
	v_fmac_f32_e32 v195, v111, v249
	v_fmac_f32_e32 v196, v248, v82
	v_fmac_f32_e32 v197, v249, v83
	ds_read_b128 v[246:249], v163
	s_waitcnt lgkmcnt(1)
	v_fmac_f32_e32 v194, v120, v234
	v_fmac_f32_e32 v195, v121, v235
	v_fmac_f32_e32 v196, v234, v92
	v_fmac_f32_e32 v197, v235, v93
	v_fmac_f32_e32 v194, v118, v236
	v_fmac_f32_e32 v195, v119, v237
	v_fmac_f32_e32 v196, v236, v90
	v_fmac_f32_e32 v197, v237, v91
	s_waitcnt lgkmcnt(0)
	v_fmac_f32_e32 v194, v124, v246
	v_fmac_f32_e32 v195, v125, v247
	v_fmac_f32_e32 v196, v246, v100
	v_fmac_f32_e32 v197, v247, v101
	v_fmac_f32_e32 v194, v122, v248
	v_fmac_f32_e32 v195, v123, v249
	v_fmac_f32_e32 v196, v248, v98
	v_fmac_f32_e32 v197, v249, v99
	v_fmac_f32_e32 v194, v130, v242
	v_fmac_f32_e32 v195, v131, v243
	v_fmac_f32_e32 v196, v242, v108
	v_fmac_f32_e32 v197, v243, v109
	v_fmac_f32_e32 v194, v126, v244
	v_fmac_f32_e32 v195, v127, v245
	v_fmac_f32_e32 v196, v244, v102
	v_fmac_f32_e32 v197, v245, v103
	ds_read_b128 v[234:237], v168
	v_fmac_f32_e32 v194, v134, v238
	v_fmac_f32_e32 v195, v135, v239
	v_fmac_f32_e32 v196, v238, v116
	v_fmac_f32_e32 v197, v239, v117
	v_fmac_f32_e32 v194, v132, v240
	v_fmac_f32_e32 v195, v133, v241
	v_fmac_f32_e32 v196, v240, v112
	v_fmac_f32_e32 v197, v241, v113
	ds_read_b128 v[238:241], v169
	v_add_f32_e32 v233, v194, v195
	v_add_f32_e32 v246, v196, v197
	s_waitcnt lgkmcnt(1)
	v_fma_f32 v194, v88, v234, 0
	v_fma_f32 v195, v89, v235, 0
	v_fma_f32 v196, v234, v72, 0
	v_fma_f32 v197, v235, v73, 0
	v_fmac_f32_e32 v194, v84, v236
	v_fmac_f32_e32 v195, v85, v237
	v_fmac_f32_e32 v196, v236, v70
	v_fmac_f32_e32 v197, v237, v71
	ds_read_b128 v[234:237], v170
	s_waitcnt lgkmcnt(1)
	v_fmac_f32_e32 v194, v96, v238
	v_fmac_f32_e32 v195, v97, v239
	v_fmac_f32_e32 v196, v238, v76
	v_fmac_f32_e32 v197, v239, v77
	v_fmac_f32_e32 v194, v94, v240
	v_fmac_f32_e32 v195, v95, v241
	v_fmac_f32_e32 v196, v240, v74
	v_fmac_f32_e32 v197, v241, v75
	ds_read_b128 v[238:241], v171
	s_waitcnt lgkmcnt(1)
	v_fmac_f32_e32 v194, v106, v234
	v_fmac_f32_e32 v195, v107, v235
	v_fmac_f32_e32 v196, v234, v80
	v_fmac_f32_e32 v197, v235, v81
	v_fmac_f32_e32 v194, v104, v236
	v_fmac_f32_e32 v195, v105, v237
	v_fmac_f32_e32 v196, v236, v78
	v_fmac_f32_e32 v197, v237, v79
	ds_read_b128 v[234:237], v172
	s_waitcnt lgkmcnt(1)
	v_fmac_f32_e32 v194, v114, v238
	v_fmac_f32_e32 v195, v115, v239
	v_fmac_f32_e32 v196, v238, v86
	v_fmac_f32_e32 v197, v239, v87
	v_fmac_f32_e32 v194, v110, v240
	v_fmac_f32_e32 v195, v111, v241
	v_fmac_f32_e32 v196, v240, v82
	v_fmac_f32_e32 v197, v241, v83
	ds_read_b128 v[238:241], v173
	s_waitcnt lgkmcnt(1)
	v_fmac_f32_e32 v194, v120, v234
	v_fmac_f32_e32 v195, v121, v235
	v_fmac_f32_e32 v196, v234, v92
	v_fmac_f32_e32 v197, v235, v93
	v_fmac_f32_e32 v194, v118, v236
	v_fmac_f32_e32 v195, v119, v237
	v_fmac_f32_e32 v196, v236, v90
	v_fmac_f32_e32 v197, v237, v91
	ds_read_b128 v[234:237], v174
	s_waitcnt lgkmcnt(1)
	v_fmac_f32_e32 v194, v124, v238
	v_fmac_f32_e32 v195, v125, v239
	v_fmac_f32_e32 v196, v238, v100
	v_fmac_f32_e32 v197, v239, v101
	v_fmac_f32_e32 v194, v122, v240
	v_fmac_f32_e32 v195, v123, v241
	v_fmac_f32_e32 v196, v240, v98
	v_fmac_f32_e32 v197, v241, v99
	ds_read_b128 v[238:241], v175
	s_waitcnt lgkmcnt(1)
	v_fmac_f32_e32 v194, v130, v234
	v_fmac_f32_e32 v195, v131, v235
	v_fmac_f32_e32 v196, v234, v108
	v_fmac_f32_e32 v197, v235, v109
	v_fmac_f32_e32 v194, v126, v236
	v_fmac_f32_e32 v195, v127, v237
	v_fmac_f32_e32 v196, v236, v102
	v_fmac_f32_e32 v197, v237, v103
	s_waitcnt lgkmcnt(0)
	v_fmac_f32_e32 v194, v134, v238
	v_fmac_f32_e32 v195, v135, v239
	v_fmac_f32_e32 v196, v238, v116
	v_fmac_f32_e32 v197, v239, v117
	v_fmac_f32_e32 v194, v132, v240
	v_fmac_f32_e32 v195, v133, v241
	v_fmac_f32_e32 v196, v240, v112
	v_fmac_f32_e32 v197, v241, v113
	ds_read_b128 v[234:237], v177
	ds_read_b128 v[238:241], v176
	ds_read_b128 v[242:245], v183
	v_add_f32_e32 v247, v194, v195
	v_add_f32_e32 v248, v196, v197
	s_waitcnt lgkmcnt(2)
	v_fma_f32 v194, v88, v234, 0
	v_fma_f32 v195, v89, v235, 0
	v_fma_f32 v196, v234, v72, 0
	v_fma_f32 v197, v235, v73, 0
	v_fmac_f32_e32 v194, v84, v236
	v_fmac_f32_e32 v195, v85, v237
	v_fmac_f32_e32 v196, v236, v70
	v_fmac_f32_e32 v197, v237, v71
	ds_read_b128 v[234:237], v182
	s_waitcnt lgkmcnt(1)
	v_fmac_f32_e32 v194, v96, v242
	v_fmac_f32_e32 v195, v97, v243
	v_fmac_f32_e32 v196, v242, v76
	v_fmac_f32_e32 v197, v243, v77
	v_fmac_f32_e32 v194, v94, v244
	v_fmac_f32_e32 v195, v95, v245
	v_fmac_f32_e32 v196, v244, v74
	v_fmac_f32_e32 v197, v245, v75
	ds_read_b128 v[242:245], v181
	s_waitcnt lgkmcnt(1)
	v_fmac_f32_e32 v194, v106, v234
	v_fmac_f32_e32 v195, v107, v235
	v_fmac_f32_e32 v196, v234, v80
	v_fmac_f32_e32 v197, v235, v81
	v_fmac_f32_e32 v194, v104, v236
	v_fmac_f32_e32 v195, v105, v237
	v_fmac_f32_e32 v196, v236, v78
	v_fmac_f32_e32 v197, v237, v79
	ds_read_b128 v[234:237], v180
	s_waitcnt lgkmcnt(1)
	v_fmac_f32_e32 v194, v114, v242
	v_fmac_f32_e32 v195, v115, v243
	v_fmac_f32_e32 v196, v242, v86
	v_fmac_f32_e32 v197, v243, v87
	v_fmac_f32_e32 v194, v110, v244
	v_fmac_f32_e32 v195, v111, v245
	v_fmac_f32_e32 v196, v244, v82
	v_fmac_f32_e32 v197, v245, v83
	ds_read_b128 v[242:245], v179
	s_waitcnt lgkmcnt(1)
	v_fmac_f32_e32 v194, v120, v234
	v_fmac_f32_e32 v195, v121, v235
	v_fmac_f32_e32 v196, v234, v92
	v_fmac_f32_e32 v197, v235, v93
	v_fmac_f32_e32 v194, v118, v236
	v_fmac_f32_e32 v195, v119, v237
	v_fmac_f32_e32 v196, v236, v90
	v_fmac_f32_e32 v197, v237, v91
	ds_read_b128 v[234:237], v178
	s_waitcnt lgkmcnt(1)
	v_fmac_f32_e32 v194, v124, v242
	v_fmac_f32_e32 v195, v125, v243
	v_fmac_f32_e32 v196, v242, v100
	v_fmac_f32_e32 v197, v243, v101
	v_fmac_f32_e32 v194, v122, v244
	v_fmac_f32_e32 v195, v123, v245
	v_fmac_f32_e32 v196, v244, v98
	v_fmac_f32_e32 v197, v245, v99
	s_waitcnt lgkmcnt(0)
	v_fmac_f32_e32 v194, v130, v234
	v_fmac_f32_e32 v195, v131, v235
	v_fmac_f32_e32 v196, v234, v108
	v_fmac_f32_e32 v197, v235, v109
	v_fmac_f32_e32 v194, v126, v236
	v_fmac_f32_e32 v195, v127, v237
	v_fmac_f32_e32 v196, v236, v102
	v_fmac_f32_e32 v197, v237, v103
	ds_read_b128 v[234:237], v184
	v_fmac_f32_e32 v194, v134, v238
	v_fmac_f32_e32 v195, v135, v239
	v_fmac_f32_e32 v196, v238, v116
	v_fmac_f32_e32 v197, v239, v117
	v_fmac_f32_e32 v194, v132, v240
	v_fmac_f32_e32 v195, v133, v241
	v_fmac_f32_e32 v196, v240, v112
	v_fmac_f32_e32 v197, v241, v113
	ds_read_b128 v[238:241], v185
	v_add_f32_e32 v244, v194, v195
	v_add_f32_e32 v245, v196, v197
	s_waitcnt lgkmcnt(1)
	v_fma_f32 v194, v88, v234, 0
	v_fma_f32 v195, v89, v235, 0
	v_fma_f32 v196, v234, v72, 0
	v_fma_f32 v197, v235, v73, 0
	v_fmac_f32_e32 v194, v84, v236
	v_fmac_f32_e32 v195, v85, v237
	v_fmac_f32_e32 v196, v236, v70
	v_fmac_f32_e32 v197, v237, v71
	ds_read_b128 v[234:237], v186
	s_waitcnt lgkmcnt(1)
	v_fmac_f32_e32 v194, v96, v238
	v_fmac_f32_e32 v195, v97, v239
	v_fmac_f32_e32 v196, v238, v76
	v_fmac_f32_e32 v197, v239, v77
	v_fmac_f32_e32 v194, v94, v240
	v_fmac_f32_e32 v195, v95, v241
	v_fmac_f32_e32 v196, v240, v74
	v_fmac_f32_e32 v197, v241, v75
	ds_read_b128 v[238:241], v187
	s_waitcnt lgkmcnt(1)
	v_fmac_f32_e32 v194, v106, v234
	v_fmac_f32_e32 v195, v107, v235
	v_fmac_f32_e32 v196, v234, v80
	v_fmac_f32_e32 v197, v235, v81
	v_fmac_f32_e32 v194, v104, v236
	v_fmac_f32_e32 v195, v105, v237
	v_fmac_f32_e32 v196, v236, v78
	v_fmac_f32_e32 v197, v237, v79
	ds_read_b128 v[234:237], v188
	s_waitcnt lgkmcnt(1)
	v_fmac_f32_e32 v194, v114, v238
	v_fmac_f32_e32 v195, v115, v239
	v_fmac_f32_e32 v196, v238, v86
	v_fmac_f32_e32 v197, v239, v87
	v_fmac_f32_e32 v194, v110, v240
	v_fmac_f32_e32 v195, v111, v241
	v_fmac_f32_e32 v196, v240, v82
	v_fmac_f32_e32 v197, v241, v83
	ds_read_b128 v[238:241], v189
	s_waitcnt lgkmcnt(1)
	v_fmac_f32_e32 v194, v120, v234
	v_fmac_f32_e32 v195, v121, v235
	v_fmac_f32_e32 v196, v234, v92
	v_fmac_f32_e32 v197, v235, v93
	v_fmac_f32_e32 v194, v118, v236
	v_fmac_f32_e32 v195, v119, v237
	v_fmac_f32_e32 v196, v236, v90
	v_fmac_f32_e32 v197, v237, v91
	ds_read_b128 v[234:237], v190
	s_waitcnt lgkmcnt(1)
	v_fmac_f32_e32 v194, v124, v238
	v_fmac_f32_e32 v195, v125, v239
	v_fmac_f32_e32 v196, v238, v100
	v_fmac_f32_e32 v197, v239, v101
	v_fmac_f32_e32 v194, v122, v240
	v_fmac_f32_e32 v195, v123, v241
	v_fmac_f32_e32 v196, v240, v98
	v_fmac_f32_e32 v197, v241, v99
	ds_read_b128 v[238:241], v191
	s_waitcnt lgkmcnt(1)
	v_fmac_f32_e32 v194, v130, v234
	v_fmac_f32_e32 v195, v131, v235
	v_fmac_f32_e32 v196, v234, v108
	v_fmac_f32_e32 v197, v235, v109
	v_fmac_f32_e32 v194, v126, v236
	v_fmac_f32_e32 v195, v127, v237
	v_fmac_f32_e32 v196, v236, v102
	v_fmac_f32_e32 v197, v237, v103
	ds_read_b128 v[234:237], v193
	s_waitcnt lgkmcnt(1)
	v_fmac_f32_e32 v194, v134, v238
	v_fmac_f32_e32 v195, v135, v239
	v_fmac_f32_e32 v196, v238, v116
	v_fmac_f32_e32 v197, v239, v117
	v_fmac_f32_e32 v194, v132, v240
	v_fmac_f32_e32 v195, v133, v241
	v_fmac_f32_e32 v196, v240, v112
	v_fmac_f32_e32 v197, v241, v113
	ds_read_b128 v[238:241], v203
	v_add_f32_e32 v249, v194, v195
	s_waitcnt lgkmcnt(1)
	v_fma_f32 v194, v88, v234, 0
	v_fma_f32 v195, v89, v235, 0
	v_fma_f32 v234, v234, v72, 0
	v_fma_f32 v235, v235, v73, 0
	v_fmac_f32_e32 v194, v84, v236
	v_fmac_f32_e32 v195, v85, v237
	v_fma_f32 v242, v236, v70, v234
	v_fma_f32 v243, v237, v71, v235
	ds_read_b128 v[234:237], v202
	s_waitcnt lgkmcnt(1)
	v_fmac_f32_e32 v194, v96, v238
	v_fmac_f32_e32 v195, v97, v239
	v_fma_f32 v238, v238, v76, v242
	v_fma_f32 v239, v239, v77, v243
	v_fmac_f32_e32 v194, v94, v240
	v_fmac_f32_e32 v195, v95, v241
	v_fma_f32 v242, v240, v74, v238
	v_fma_f32 v243, v241, v75, v239
	ds_read_b128 v[238:241], v201
	s_waitcnt lgkmcnt(1)
	v_fmac_f32_e32 v194, v106, v234
	v_fmac_f32_e32 v195, v107, v235
	v_fma_f32 v234, v234, v80, v242
	v_fma_f32 v235, v235, v81, v243
	v_fmac_f32_e32 v194, v104, v236
	v_fmac_f32_e32 v195, v105, v237
	v_fma_f32 v242, v236, v78, v234
	v_fma_f32 v243, v237, v79, v235
	ds_read_b128 v[234:237], v200
	s_waitcnt lgkmcnt(1)
	v_fmac_f32_e32 v194, v114, v238
	v_fmac_f32_e32 v195, v115, v239
	v_fma_f32 v238, v238, v86, v242
	v_fma_f32 v239, v239, v87, v243
	v_fmac_f32_e32 v194, v110, v240
	v_fmac_f32_e32 v195, v111, v241
	v_fma_f32 v242, v240, v82, v238
	v_fma_f32 v243, v241, v83, v239
	ds_read_b128 v[238:241], v199
	s_waitcnt lgkmcnt(1)
	v_fmac_f32_e32 v194, v120, v234
	v_fmac_f32_e32 v195, v121, v235
	v_fma_f32 v234, v234, v92, v242
	v_fma_f32 v235, v235, v93, v243
	v_fmac_f32_e32 v194, v118, v236
	v_fmac_f32_e32 v195, v119, v237
	v_fma_f32 v242, v236, v90, v234
	v_fma_f32 v243, v237, v91, v235
	ds_read_b128 v[234:237], v198
	s_waitcnt lgkmcnt(1)
	v_fmac_f32_e32 v194, v124, v238
	v_fmac_f32_e32 v195, v125, v239
	v_fma_f32 v238, v238, v100, v242
	v_fma_f32 v239, v239, v101, v243
	v_fmac_f32_e32 v194, v122, v240
	v_fmac_f32_e32 v195, v123, v241
	v_fma_f32 v242, v240, v98, v238
	v_fma_f32 v243, v241, v99, v239
	ds_read_b128 v[238:241], v192
	v_add_f32_e32 v231, v196, v197
	s_waitcnt lgkmcnt(1)
	v_fmac_f32_e32 v194, v130, v234
	v_fmac_f32_e32 v195, v131, v235
	v_fma_f32 v196, v234, v108, v242
	v_fma_f32 v197, v235, v109, v243
	v_cndmask_b32_e64 v234, v128, v136, s[58:59]
	v_cndmask_b32_e64 v128, v136, v128, s[58:59]
	v_cndmask_b32_e64 v136, v137, v138, s[58:59]
	ds_bpermute_b32 v136, v140, v136
	v_fmac_f32_e32 v194, v126, v236
	v_fmac_f32_e32 v195, v127, v237
	v_fmac_f32_e32 v196, v236, v102
	v_fmac_f32_e32 v197, v237, v103
	s_waitcnt lgkmcnt(1)
	v_fmac_f32_e32 v194, v134, v238
	v_fmac_f32_e32 v195, v135, v239
	v_fmac_f32_e32 v196, v238, v116
	v_fmac_f32_e32 v197, v239, v117
	v_fmac_f32_e32 v194, v132, v240
	v_fmac_f32_e32 v195, v133, v241
	v_fmac_f32_e32 v196, v240, v112
	v_fmac_f32_e32 v197, v241, v113
	v_cndmask_b32_e64 v137, v138, v137, s[58:59]
	v_cndmask_b32_e64 v138, v139, v213, s[58:59]
	v_add_f32_e32 v194, v194, v195
	v_add_f32_e32 v195, v196, v197
	ds_bpermute_b32 v138, v140, v138
	v_cndmask_b32_e64 v196, v214, v215, s[58:59]
	ds_bpermute_b32 v196, v140, v196
	s_waitcnt lgkmcnt(2)
	v_add_f32_e32 v136, v137, v136
	v_cndmask_b32_e64 v137, v213, v139, s[58:59]
	v_cndmask_b32_e64 v139, v216, v217, s[58:59]
	ds_bpermute_b32 v139, v140, v139
	v_cndmask_b32_e64 v197, v218, v219, s[58:59]
	ds_bpermute_b32 v197, v140, v197
	v_cndmask_b32_e64 v213, v220, v221, s[58:59]
	ds_bpermute_b32 v213, v140, v213
	s_waitcnt lgkmcnt(4)
	v_add_f32_e32 v137, v137, v138
	v_cndmask_b32_e64 v138, v215, v214, s[58:59]
	s_waitcnt lgkmcnt(3)
	v_add_f32_e32 v138, v138, v196
	v_cndmask_b32_e64 v196, v217, v216, s[58:59]
	s_waitcnt lgkmcnt(2)
	v_add_f32_e32 v139, v196, v139
	v_cndmask_b32_e64 v196, v219, v218, s[58:59]
	s_waitcnt lgkmcnt(1)
	v_add_f32_e32 v196, v196, v197
	v_cndmask_b32_e64 v197, v221, v220, s[58:59]
	s_waitcnt lgkmcnt(0)
	v_add_f32_e32 v197, v197, v213
	v_cndmask_b32_e64 v213, v222, v223, s[58:59]
	ds_bpermute_b32 v213, v140, v213
	v_cndmask_b32_e64 v215, v224, v225, s[58:59]
	ds_bpermute_b32 v215, v140, v215
	v_cndmask_b32_e64 v216, v226, v227, s[58:59]
	ds_bpermute_b32 v216, v140, v216
	v_cndmask_b32_e64 v214, v223, v222, s[58:59]
	ds_bpermute_b32 v234, v140, v234
	s_waitcnt lgkmcnt(3)
	v_add_f32_e32 v213, v214, v213
	v_cndmask_b32_e64 v214, v225, v224, s[58:59]
	s_waitcnt lgkmcnt(2)
	v_add_f32_e32 v214, v214, v215
	v_cndmask_b32_e64 v215, v227, v226, s[58:59]
	s_waitcnt lgkmcnt(1)
	v_add_f32_e32 v215, v215, v216
	v_cndmask_b32_e64 v216, v228, v229, s[58:59]
	ds_bpermute_b32 v216, v140, v216
	v_cndmask_b32_e64 v218, v233, v246, s[58:59]
	ds_bpermute_b32 v218, v140, v218
	v_cndmask_b32_e64 v219, v247, v248, s[58:59]
	s_waitcnt lgkmcnt(2)
	v_add_f32_e32 v128, v128, v234
	ds_bpermute_b32 v219, v140, v219
	v_cndmask_b32_e64 v222, v194, v195, s[58:59]
	v_cndmask_b32_e64 v194, v195, v194, s[58:59]
	v_cndmask_b32_e64 v195, v128, v214, s[60:61]
	v_cndmask_b32_e64 v128, v214, v128, s[60:61]
	v_cndmask_b32_e64 v214, v136, v215, s[60:61]
	v_cndmask_b32_e64 v217, v229, v228, s[58:59]
	ds_bpermute_b32 v195, v141, v195
	ds_bpermute_b32 v214, v141, v214
	s_waitcnt lgkmcnt(4)
	v_add_f32_e32 v216, v217, v216
	v_cndmask_b32_e64 v217, v246, v233, s[58:59]
	s_waitcnt lgkmcnt(3)
	v_add_f32_e32 v217, v217, v218
	v_cndmask_b32_e64 v218, v248, v247, s[58:59]
	s_waitcnt lgkmcnt(2)
	v_add_f32_e32 v218, v218, v219
	v_cndmask_b32_e64 v219, v244, v245, s[58:59]
	ds_bpermute_b32 v219, v140, v219
	v_cndmask_b32_e64 v221, v249, v231, s[58:59]
	v_cndmask_b32_e64 v136, v215, v136, s[60:61]
	ds_bpermute_b32 v221, v140, v221
	ds_bpermute_b32 v222, v140, v222
	s_waitcnt lgkmcnt(4)
	v_add_f32_e32 v128, v128, v195
	s_waitcnt lgkmcnt(3)
	v_add_f32_e32 v136, v136, v214
	v_cndmask_b32_e64 v195, v138, v217, s[60:61]
	v_cndmask_b32_e64 v214, v139, v218, s[60:61]
	ds_bpermute_b32 v195, v141, v195
	ds_bpermute_b32 v214, v141, v214
	v_cndmask_b32_e64 v220, v245, v244, s[58:59]
	s_waitcnt lgkmcnt(4)
	v_add_f32_e32 v219, v220, v219
	v_cndmask_b32_e64 v220, v231, v249, s[58:59]
	s_waitcnt lgkmcnt(3)
	v_add_f32_e32 v220, v220, v221
	s_waitcnt lgkmcnt(2)
	v_add_f32_e32 v194, v194, v222
	v_cndmask_b32_e64 v138, v217, v138, s[60:61]
	v_cndmask_b32_e64 v139, v218, v139, s[60:61]
	v_cndmask_b32_e64 v221, v137, v216, s[60:61]
	v_cndmask_b32_e64 v215, v196, v219, s[60:61]
	s_waitcnt lgkmcnt(1)
	v_add_f32_e32 v138, v138, v195
	s_waitcnt lgkmcnt(0)
	v_add_f32_e32 v139, v139, v214
	v_cndmask_b32_e64 v195, v219, v196, s[60:61]
	v_cndmask_b32_e64 v196, v197, v220, s[60:61]
	v_cndmask_b32_e64 v214, v213, v194, s[60:61]
	ds_bpermute_b32 v221, v141, v221
	ds_bpermute_b32 v215, v141, v215
	ds_bpermute_b32 v196, v141, v196
	ds_bpermute_b32 v214, v141, v214
	v_cndmask_b32_e64 v137, v216, v137, s[60:61]
	v_cndmask_b32_e64 v197, v220, v197, s[60:61]
	v_cndmask_b32_e64 v194, v194, v213, s[60:61]
	s_waitcnt lgkmcnt(3)
	v_add_f32_e32 v137, v137, v221
	s_waitcnt lgkmcnt(2)
	v_add_f32_e32 v195, v195, v215
	s_waitcnt lgkmcnt(1)
	v_add_f32_e32 v196, v197, v196
	s_waitcnt lgkmcnt(0)
	v_add_f32_e32 v194, v194, v214
	v_cndmask_b32_e64 v215, v128, v139, s[62:63]
	v_cndmask_b32_e64 v128, v139, v128, s[62:63]
	v_cndmask_b32_e64 v139, v136, v195, s[62:63]
	v_cndmask_b32_e64 v136, v195, v136, s[62:63]
	v_cndmask_b32_e64 v195, v137, v196, s[62:63]
	v_cndmask_b32_e64 v197, v138, v194, s[62:63]
	ds_bpermute_b32 v215, v142, v215
	ds_bpermute_b32 v139, v142, v139
	ds_bpermute_b32 v195, v142, v195
	ds_bpermute_b32 v197, v142, v197
	v_cndmask_b32_e64 v137, v196, v137, s[62:63]
	v_cndmask_b32_e64 v138, v194, v138, s[62:63]
	s_waitcnt lgkmcnt(3)
	v_add_f32_e32 v128, v128, v215
	s_waitcnt lgkmcnt(2)
	v_add_f32_e32 v136, v136, v139
	s_waitcnt lgkmcnt(1)
	v_add_f32_e32 v137, v137, v195
	s_waitcnt lgkmcnt(0)
	v_add_f32_e32 v138, v138, v197
	v_cndmask_b32_e64 v139, v128, v137, s[64:65]
	v_cndmask_b32_e64 v194, v136, v138, s[64:65]
	ds_bpermute_b32 v139, v143, v139
	ds_bpermute_b32 v194, v143, v194
	v_cndmask_b32_e64 v128, v137, v128, s[64:65]
	v_cndmask_b32_e64 v136, v138, v136, s[64:65]
	s_waitcnt lgkmcnt(1)
	v_add_f32_e32 v128, v128, v139
	s_waitcnt lgkmcnt(0)
	v_add_f32_e32 v136, v136, v194
	v_cndmask_b32_e64 v137, v128, v136, s[66:67]
	ds_bpermute_b32 v137, v144, v137
	v_cndmask_b32_e64 v128, v136, v128, s[66:67]
	s_waitcnt lgkmcnt(0)
	v_add_f32_e32 v128, v128, v137
	s_nop 1
	v_mov_b32_dpp v136, v128 quad_perm:[1,0,3,2] row_mask:0xf bank_mask:0xf bound_ctrl:1
	s_and_saveexec_b64 s[16:17], s[68:69]
	s_cbranch_execz .LBB0_1066
	v_add_f32_e32 v128, v128, v136
	v_mul_f32_e32 v128, 0xbfb8aa3b, v128
	v_exp_f32_e32 v128, v128
	s_nop 0
	v_add_f32_e32 v128, 1.0, v128
	v_rcp_f32_e32 v128, v128
	ds_write_b32 v204, v128
	s_branch .LBB0_1066
.LBB0_1073:
	v_mov_b32_e32 v0, v64
	s_waitcnt lgkmcnt(0)
	s_barrier
	s_nop 0
	v_cmp_gt_i32_e32 vcc, s18, v0
	s_and_saveexec_b64 s[10:11], vcc
	s_cbranch_execz .LBB0_1084
	v_add_u32_e32 v28, s19, v0
	v_mul_hi_i32 v1, v28, s53
	v_lshrrev_b32_e32 v2, 31, v1
	v_ashrrev_i32_e32 v1, 9, v1
	v_add_u32_e32 v1, v1, v2
	v_mul_i32_i24_e32 v1, 0x900, v1
	v_sub_u32_e32 v1, v28, v1
	v_cmp_lt_i32_e32 vcc, s79, v1
	s_xor_b64 s[2:3], s[0:1], -1
	s_or_b64 s[2:3], s[2:3], vcc
	s_and_b64 exec, exec, s[2:3]
	s_cbranch_execz .LBB0_1084
	s_load_dwordx2 s[2:3], s[8:9], 0xb0
	v_mov_b32_e32 v29, 0
	v_lshl_add_u32 v0, v0, 6, 0
	v_add_u32_e32 v0, 0x20000, v0
	s_waitcnt lgkmcnt(0)
	global_load_dwordx4 v[4:7], v29, s[2:3] offset:48
	global_load_dwordx4 v[12:15], v29, s[2:3] offset:32
	global_load_dwordx4 v[20:23], v29, s[2:3] offset:16
	global_load_dwordx4 v[30:33], v29, s[2:3]
	ds_read_b128 v[24:27], v0
	ds_read_b128 v[16:19], v0 offset:16
	ds_read_b128 v[8:11], v0 offset:32
	ds_read_b128 v[0:3], v0 offset:48
	s_waitcnt vmcnt(0) lgkmcnt(3)
	v_add_f32_e32 v34, v30, v24
	v_add_f32_e32 v35, v31, v25
	s_nop 0
	v_cmp_gt_f32_e32 vcc, v35, v34
	v_add_f32_e32 v30, v32, v26
	v_add_f32_e32 v32, v33, v27
	v_cndmask_b32_e32 v33, v34, v35, vcc
	v_cmp_gt_f32_e64 s[58:59], v30, v33
	v_cndmask_b32_e64 v31, 0, 1, vcc
	s_nop 0
	v_cndmask_b32_e64 v36, v33, v30, s[58:59]
	v_cndmask_b32_e64 v31, v31, 2, s[58:59]
	v_cmp_ngt_f32_e64 s[60:61], v32, v36
	s_nop 1
	v_cndmask_b32_e64 v33, 3, v31, s[60:61]
	v_mov_b32_e32 v31, 0xff800000
	v_cmp_ne_u32_e64 s[62:63], 0, v33
	v_cmp_lg_f32_e64 s[64:65], v34, v31
	s_and_b64 s[62:63], s[62:63], s[64:65]
	v_cndmask_b32_e64 v34, v31, v34, s[62:63]
	v_cmp_ne_u32_e64 s[64:65], 1, v33
	v_cmp_gt_f32_e64 s[66:67], v35, v34
	s_and_b64 s[64:65], s[64:65], s[66:67]
	v_cndmask_b32_e64 v34, v34, v35, s[64:65]
	v_cmp_ne_u32_e64 s[66:67], 2, v33
	v_cmp_gt_f32_e64 s[68:69], v30, v34
	s_and_b64 s[66:67], s[66:67], s[68:69]
	v_cndmask_b32_e64 v30, v34, v30, s[66:67]
	v_cmp_gt_f32_e64 s[68:69], v32, v30
	s_and_b64 s[68:69], s[60:61], s[68:69]
	v_cndmask_b32_e64 v36, v32, v36, s[60:61]
	v_cndmask_b32_e64 v30, v30, v32, s[68:69]
	v_add_f32_e32 v35, v36, v30
	v_cmp_lg_f32_e64 s[70:71], v35, v31
	v_mov_b32_e32 v32, 0
	v_mov_b32_e32 v30, 0
	v_mov_b32_e32 v34, 0
	s_and_saveexec_b64 s[8:9], s[70:71]
	s_cbranch_execz .LBB0_1077
	v_cndmask_b32_e64 v29, 0, v24, s[62:63]
	v_cndmask_b32_e64 v29, v29, v25, s[64:65]
	v_cndmask_b32_e64 v30, 0, 1, s[64:65]
	v_cndmask_b32_e32 v24, v24, v25, vcc
	v_cndmask_b32_e64 v29, v29, v26, s[66:67]
	v_cndmask_b32_e64 v30, v30, 2, s[66:67]
	v_cndmask_b32_e64 v24, v24, v26, s[58:59]
	v_cndmask_b32_e64 v29, v29, v27, s[68:69]
	v_cndmask_b32_e64 v30, v30, 3, s[68:69]
	v_cndmask_b32_e64 v32, v27, v24, s[60:61]
	v_mov_b32_e32 v31, v35
	v_mov_b32_e32 v34, v33
.LBB0_1077:
	s_or_b64 exec, exec, s[8:9]
	s_waitcnt lgkmcnt(2)
	v_add_f32_e32 v24, v20, v16
	v_add_f32_e32 v25, v21, v17
	v_add_f32_e32 v21, v22, v18
	v_cmp_gt_f32_e32 vcc, v25, v24
	v_add_f32_e32 v22, v23, v19
	s_mov_b32 s2, 0xff800000
	v_cndmask_b32_e32 v23, v24, v25, vcc
	v_cmp_gt_f32_e64 s[58:59], v21, v23
	v_cndmask_b32_e64 v20, 0, 1, vcc
	v_cmp_lg_f32_e64 s[64:65], s2, v24
	v_cndmask_b32_e64 v23, v23, v21, s[58:59]
	v_cndmask_b32_e64 v20, v20, 2, s[58:59]
	v_cmp_ngt_f32_e64 s[60:61], v22, v23
	v_mov_b32_e32 v26, 0xff800000
	s_nop 0
	v_cndmask_b32_e64 v20, 3, v20, s[60:61]
	v_cmp_ne_u32_e64 s[62:63], 0, v20
	s_and_b64 s[62:63], s[62:63], s[64:65]
	v_cmp_ne_u32_e64 s[64:65], 1, v20
	v_cndmask_b32_e64 v24, v26, v24, s[62:63]
	v_cmp_gt_f32_e64 s[66:67], v25, v24
	s_and_b64 s[64:65], s[64:65], s[66:67]
	v_cndmask_b32_e64 v24, v24, v25, s[64:65]
	v_cmp_ne_u32_e64 s[66:67], 2, v20
	v_cmp_gt_f32_e64 s[68:69], v21, v24
	s_and_b64 s[66:67], s[66:67], s[68:69]
	v_cndmask_b32_e64 v21, v24, v21, s[66:67]
	v_cmp_gt_f32_e64 s[68:69], v22, v21
	s_and_b64 s[68:69], s[60:61], s[68:69]
	v_cndmask_b32_e64 v23, v22, v23, s[60:61]
	v_cndmask_b32_e64 v21, v21, v22, s[68:69]
	v_add_f32_e32 v21, v23, v21
	v_cmp_gt_f32_e64 s[70:71], v21, v31
	s_and_saveexec_b64 s[8:9], s[70:71]
	s_cbranch_execz .LBB0_1079
	v_or_b32_e32 v34, 4, v20
	v_cndmask_b32_e64 v20, 0, v16, s[62:63]
	v_cndmask_b32_e64 v22, 4, 5, s[64:65]
	v_cndmask_b32_e64 v20, v20, v17, s[64:65]
	v_cndmask_b32_e32 v16, v16, v17, vcc
	v_cndmask_b32_e64 v22, v22, 6, s[66:67]
	v_cndmask_b32_e64 v20, v20, v18, s[66:67]
	v_cndmask_b32_e64 v16, v16, v18, s[58:59]
	v_cndmask_b32_e64 v30, v22, 7, s[68:69]
	v_cndmask_b32_e64 v29, v20, v19, s[68:69]
	v_cndmask_b32_e64 v32, v19, v16, s[60:61]
	v_mov_b32_e32 v31, v21
.LBB0_1079:
	s_or_b64 exec, exec, s[8:9]
	s_waitcnt lgkmcnt(1)
	v_add_f32_e32 v16, v12, v8
	v_add_f32_e32 v17, v13, v9
	v_add_f32_e32 v13, v14, v10
	v_cmp_gt_f32_e32 vcc, v17, v16
	v_add_f32_e32 v14, v15, v11
	v_cmp_lg_f32_e64 s[64:65], s2, v16
	v_cndmask_b32_e32 v15, v16, v17, vcc
	v_cmp_gt_f32_e64 s[58:59], v13, v15
	v_cndmask_b32_e64 v12, 0, 1, vcc
	v_mov_b32_e32 v18, 0xff800000
	v_cndmask_b32_e64 v15, v15, v13, s[58:59]
	v_cndmask_b32_e64 v12, v12, 2, s[58:59]
	v_cmp_ngt_f32_e64 s[60:61], v14, v15
	s_nop 1
	v_cndmask_b32_e64 v12, 3, v12, s[60:61]
	v_cmp_ne_u32_e64 s[62:63], 0, v12
	s_and_b64 s[62:63], s[62:63], s[64:65]
	v_cmp_ne_u32_e64 s[64:65], 1, v12
	v_cndmask_b32_e64 v16, v18, v16, s[62:63]
	v_cmp_gt_f32_e64 s[66:67], v17, v16
	s_and_b64 s[64:65], s[64:65], s[66:67]
	v_cndmask_b32_e64 v16, v16, v17, s[64:65]
	v_cmp_ne_u32_e64 s[66:67], 2, v12
	v_cmp_gt_f32_e64 s[68:69], v13, v16
	s_and_b64 s[66:67], s[66:67], s[68:69]
	v_cndmask_b32_e64 v13, v16, v13, s[66:67]
	v_cmp_gt_f32_e64 s[68:69], v14, v13
	s_and_b64 s[68:69], s[60:61], s[68:69]
	v_cndmask_b32_e64 v15, v14, v15, s[60:61]
	v_cndmask_b32_e64 v13, v13, v14, s[68:69]
	v_add_f32_e32 v13, v15, v13
	v_cmp_gt_f32_e64 s[70:71], v13, v31
	s_and_saveexec_b64 s[8:9], s[70:71]
	s_cbranch_execz .LBB0_1081
	v_or_b32_e32 v34, 8, v12
	v_cndmask_b32_e64 v12, 0, v8, s[62:63]
	v_cndmask_b32_e64 v14, 8, 9, s[64:65]
	v_cndmask_b32_e64 v12, v12, v9, s[64:65]
	v_cndmask_b32_e32 v8, v8, v9, vcc
	v_cndmask_b32_e64 v14, v14, 10, s[66:67]
	v_cndmask_b32_e64 v12, v12, v10, s[66:67]
	v_cndmask_b32_e64 v8, v8, v10, s[58:59]
	v_cndmask_b32_e64 v30, v14, 11, s[68:69]
	v_cndmask_b32_e64 v29, v12, v11, s[68:69]
	v_cndmask_b32_e64 v32, v11, v8, s[60:61]
	v_mov_b32_e32 v31, v13
.LBB0_1081:
	s_or_b64 exec, exec, s[8:9]
	s_waitcnt lgkmcnt(0)
	v_add_f32_e32 v8, v4, v0
	v_add_f32_e32 v9, v5, v1
	v_add_f32_e32 v5, v6, v2
	v_cmp_gt_f32_e32 vcc, v9, v8
	v_add_f32_e32 v6, v7, v3
	v_cmp_lg_f32_e64 s[64:65], s2, v8
	v_cndmask_b32_e32 v7, v8, v9, vcc
	v_cmp_gt_f32_e64 s[58:59], v5, v7
	v_cndmask_b32_e64 v4, 0, 1, vcc
	v_mov_b32_e32 v10, 0xff800000
	v_cndmask_b32_e64 v7, v7, v5, s[58:59]
	v_cndmask_b32_e64 v4, v4, 2, s[58:59]
	v_cmp_ngt_f32_e64 s[60:61], v6, v7
	s_nop 1
	v_cndmask_b32_e64 v4, 3, v4, s[60:61]
	v_cmp_ne_u32_e64 s[62:63], 0, v4
	s_and_b64 s[62:63], s[62:63], s[64:65]
	v_cmp_ne_u32_e64 s[64:65], 1, v4
	v_cndmask_b32_e64 v8, v10, v8, s[62:63]
	v_cmp_gt_f32_e64 s[66:67], v9, v8
	s_and_b64 s[64:65], s[64:65], s[66:67]
	v_cndmask_b32_e64 v8, v8, v9, s[64:65]
	v_cmp_ne_u32_e64 s[66:67], 2, v4
	v_cmp_gt_f32_e64 s[68:69], v5, v8
	s_and_b64 s[66:67], s[66:67], s[68:69]
	v_cndmask_b32_e64 v5, v8, v5, s[66:67]
	v_cmp_gt_f32_e64 s[68:69], v6, v5
	s_and_b64 s[68:69], s[60:61], s[68:69]
	v_cndmask_b32_e64 v7, v6, v7, s[60:61]
	v_cndmask_b32_e64 v5, v5, v6, s[68:69]
	v_add_f32_e32 v5, v7, v5
	v_cmp_gt_f32_e64 s[70:71], v5, v31
	s_and_saveexec_b64 s[8:9], s[70:71]
	s_cbranch_execz .LBB0_1083
	v_or_b32_e32 v34, 12, v4
	v_cndmask_b32_e64 v4, 0, v0, s[62:63]
	v_cndmask_b32_e64 v5, 12, 13, s[64:65]
	v_cndmask_b32_e64 v4, v4, v1, s[64:65]
	v_cndmask_b32_e32 v0, v0, v1, vcc
	v_cndmask_b32_e64 v5, v5, 14, s[66:67]
	v_cndmask_b32_e64 v4, v4, v2, s[66:67]
	v_cndmask_b32_e64 v0, v0, v2, s[58:59]
	v_cndmask_b32_e64 v30, v5, 15, s[68:69]
	v_cndmask_b32_e64 v29, v4, v3, s[68:69]
	v_cndmask_b32_e64 v32, v3, v0, s[60:61]
